# LN1/LN2 wave reductions via DPP+permlane swaps (no ds_bpermute); router bias loaded once per phase instead of 8 serialized flat loads per row pair; on top of router loop rewrite
# speedup vs baseline: 1.0046x; 1.0028x over previous
; #define GAS __attribute__((address_space(1)))
; #define LAS __attribute__((address_space(3)))
; __device__ __forceinline__ void ln1_router_phase(const Args& a, Frame& F, int l) {
;     const unsigned short* PRE = (const unsigned short*)(F.ws + WS_PRE); bf16* X1B = (bf16*)(F.ws + WS_X1B); unsigned short* X1H = (unsigned short*)(F.ws + WS_X1H);
;     const float* g = inp(F, I_LNG) + ((size_t)l * 2 + 0) * DM; const float* bta = inp(F, I_LNB) + ((size_t)l * 2 + 0) * DM;
;     const float* wr = inp(F, I_WR); const float* br = inp(F, I_BR);
;     LAS float* wl = (LAS float*)(F.lds + RING_OFF);
;     { f32x4 wv[16];
; #pragma unroll
;       for (int k = 0; k < 16; ++k) wv[k] = *(const GAS f32x4*)(wr + 4 * (F.tid + NTHR * k));
; #pragma unroll
;       for (int k = 0; k < 16; ++k) { const int i4 = F.tid + NTHR * k, c = i4 >> 2, e0 = (i4 & 3) * 4;
; #pragma unroll
;           for (int j = 0; j < 4; ++j) wl[(e0 + j) * DM + c] = wv[k][j]; } }
;     __syncthreads();
.LBB0_795:
	v_readlane_b32 s0, v249, 5
	v_readlane_b32 s1, v249, 6
	s_cmp_le_i32 s0, s8
	s_cselect_b64 s[0:1], -1, 0
	s_and_b64 s[4:5], s[0:1], s[2:3]
	s_andn2_b64 vcc, exec, s[4:5]
	s_cbranch_vccnz .LBB0_940
	s_mov_b32 s0, -1
	s_nop 0
	v_mbcnt_lo_u32_b32 v0, s0, 0
	v_mbcnt_hi_u32_b32 v0, s0, v0
	v_readlane_b32 s0, v249, 4
	s_waitcnt vmcnt(0)
	s_nop 0
	v_add_u32_e32 v66, s0, v0
	v_readlane_b32 s0, v247, 30
	s_nop 0
	v_lshlrev_b32_e32 v68, 2, v66
	v_mov_b32_e32 v0, s0
	s_waitcnt lgkmcnt(0)
	ds_read_b64 v[2:3], v0
	v_readlane_b32 s0, v247, 43
	v_ashrrev_i32_e32 v69, 31, v68
	v_add_u32_e32 v6, 0x800, v68
	v_mov_b32_e32 v0, s0
	s_waitcnt lgkmcnt(0)
	v_readfirstlane_b32 s62, v2
	v_readfirstlane_b32 s63, v3
	ds_read_b128 v[2:5], v0
	v_readlane_b32 s0, v247, 44
	v_ashrrev_i32_e32 v7, 31, v6
	v_add_u32_e32 v10, 0x1000, v68
	v_mov_b32_e32 v0, s0
	s_waitcnt lgkmcnt(0)
	v_readfirstlane_b32 s8, v2
	v_readfirstlane_b32 s10, v3
	v_readfirstlane_b32 s2, v4
	v_readfirstlane_b32 s3, v5
	ds_read_b128 v[2:5], v0
	v_ashrrev_i32_e32 v11, 31, v10
	v_add_u32_e32 v14, 0x1800, v68
	v_ashrrev_i32_e32 v15, 31, v14
	v_add_u32_e32 v18, 0x2000, v68
	s_waitcnt lgkmcnt(0)
	v_readfirstlane_b32 s0, v2
	v_readfirstlane_b32 s1, v3
	v_readfirstlane_b32 s28, v4
	v_readfirstlane_b32 s29, v5
	v_lshl_add_u64 v[2:3], v[68:69], 2, s[0:1]
	global_load_dwordx4 v[2:5], v[2:3], off
	v_lshl_add_u64 v[6:7], v[6:7], 2, s[0:1]
	global_load_dwordx4 v[6:9], v[6:7], off
	v_lshl_add_u64 v[10:11], v[10:11], 2, s[0:1]
	global_load_dwordx4 v[10:13], v[10:11], off
	v_mov_b32_e32 v147, 0
	global_load_dwordx4 v[218:221], v147, s[28:29]
	global_load_dwordx4 v[236:239], v147, s[28:29] offset:16
	global_load_dwordx4 v[240:243], v147, s[28:29] offset:32
	global_load_dwordx2 v[244:245], v147, s[28:29] offset:48
	global_load_dword v235, v147, s[28:29] offset:56
	global_load_dword v147, v147, s[28:29] offset:60
	v_lshl_add_u64 v[14:15], v[14:15], 2, s[0:1]
	global_load_dwordx4 v[14:17], v[14:15], off
	v_ashrrev_i32_e32 v19, 31, v18
	v_lshl_add_u64 v[18:19], v[18:19], 2, s[0:1]
	global_load_dwordx4 v[18:21], v[18:19], off
	v_add_u32_e32 v22, 0x2800, v68
	v_ashrrev_i32_e32 v23, 31, v22
	v_lshl_add_u64 v[22:23], v[22:23], 2, s[0:1]
	global_load_dwordx4 v[22:25], v[22:23], off
	v_add_u32_e32 v26, 0x3000, v68
	v_ashrrev_i32_e32 v27, 31, v26
	v_lshl_add_u64 v[26:27], v[26:27], 2, s[0:1]
	global_load_dwordx4 v[38:41], v[26:27], off
	v_add_u32_e32 v26, 0x3800, v68
	v_ashrrev_i32_e32 v27, 31, v26
	v_lshl_add_u64 v[26:27], v[26:27], 2, s[0:1]
	global_load_dwordx4 v[62:65], v[26:27], off
	v_add_u32_e32 v26, 0x4000, v68
	v_ashrrev_i32_e32 v27, 31, v26
	v_lshl_add_u64 v[26:27], v[26:27], 2, s[0:1]
	global_load_dwordx4 v[58:61], v[26:27], off
	v_add_u32_e32 v26, 0x4800, v68
	v_ashrrev_i32_e32 v27, 31, v26
	v_lshl_add_u64 v[26:27], v[26:27], 2, s[0:1]
	global_load_dwordx4 v[54:57], v[26:27], off
	v_add_u32_e32 v26, 0x5000, v68
	v_ashrrev_i32_e32 v27, 31, v26
	v_lshl_add_u64 v[26:27], v[26:27], 2, s[0:1]
	global_load_dwordx4 v[50:53], v[26:27], off
	v_add_u32_e32 v26, 0x5800, v68
	v_ashrrev_i32_e32 v27, 31, v26
	v_lshl_add_u64 v[26:27], v[26:27], 2, s[0:1]
	global_load_dwordx4 v[46:49], v[26:27], off
	v_add_u32_e32 v26, 0x6000, v68
	v_ashrrev_i32_e32 v27, 31, v26
	v_lshl_add_u64 v[26:27], v[26:27], 2, s[0:1]
	global_load_dwordx4 v[42:45], v[26:27], off
	v_add_u32_e32 v26, 0x6800, v68
	v_ashrrev_i32_e32 v27, 31, v26
	v_lshl_add_u64 v[26:27], v[26:27], 2, s[0:1]
	global_load_dwordx4 v[34:37], v[26:27], off
	v_add_u32_e32 v26, 0x7000, v68
	v_ashrrev_i32_e32 v27, 31, v26
	v_lshl_add_u64 v[26:27], v[26:27], 2, s[0:1]
	global_load_dwordx4 v[30:33], v[26:27], off
	v_add_u32_e32 v26, 0x7800, v68
	v_ashrrev_i32_e32 v27, 31, v26
	v_lshl_add_u64 v[26:27], v[26:27], 2, s[0:1]
	global_load_dwordx4 v[26:29], v[26:27], off
	v_lshlrev_b32_e32 v67, 15, v66
	v_and_b32_e32 v0, -4, v66
	v_and_b32_e32 v67, 0x18000, v67
	v_add3_u32 v0, 0, v0, v67
	v_readlane_b32 s0, v248, 54
	v_readlane_b32 s1, v248, 55
	v_readfirstlane_b32 s11, v66
	s_waitcnt vmcnt(15)
	ds_write2st64_b32 v0, v2, v3 offset1:32
	ds_write2st64_b32 v0, v4, v5 offset0:64 offset1:96
	v_add_u32_e32 v0, 0x200, v66
	v_and_b32_e32 v0, -4, v0
	v_add3_u32 v0, 0, v0, v67
	s_waitcnt vmcnt(14)
	ds_write2st64_b32 v0, v6, v7 offset1:32
	ds_write2st64_b32 v0, v8, v9 offset0:64 offset1:96
	v_add_u32_e32 v0, 0x400, v66
	v_and_b32_e32 v0, -4, v0
	v_add3_u32 v0, 0, v0, v67
	s_waitcnt vmcnt(13)
	ds_write2st64_b32 v0, v10, v11 offset1:32
	ds_write2st64_b32 v0, v12, v13 offset0:64 offset1:96
	v_add_u32_e32 v0, 0x600, v66
	v_and_b32_e32 v0, -4, v0
	v_add3_u32 v0, 0, v0, v67
	s_waitcnt vmcnt(12)
	ds_write2st64_b32 v0, v14, v15 offset1:32
	ds_write2st64_b32 v0, v16, v17 offset0:64 offset1:96
	v_add_u32_e32 v0, 0x800, v66
	v_and_b32_e32 v0, -4, v0
	v_add3_u32 v0, 0, v0, v67
	s_waitcnt vmcnt(11)
	ds_write2st64_b32 v0, v18, v19 offset1:32
	ds_write2st64_b32 v0, v20, v21 offset0:64 offset1:96
	v_add_u32_e32 v0, 0xa00, v66
	v_and_b32_e32 v0, -4, v0
	v_add3_u32 v0, 0, v0, v67
	s_waitcnt vmcnt(10)
	ds_write2st64_b32 v0, v22, v23 offset1:32
	ds_write2st64_b32 v0, v24, v25 offset0:64 offset1:96
	v_add_u32_e32 v0, 0xc00, v66
	v_and_b32_e32 v0, -4, v0
	v_add3_u32 v0, 0, v0, v67
	s_waitcnt vmcnt(9)
; #define LAS __attribute__((address_space(3)))
; __device__ __forceinline__ void ln1_router_phase(const Args& a, Frame& F, int l) {
;     ...
;       for (int k = 0; k < 16; ++k) { const int i4 = F.tid + NTHR * k, c = i4 >> 2, e0 = (i4 & 3) * 4;
; #pragma unroll
;           for (int j = 0; j < 4; ++j) wl[(e0 + j) * DM + c] = wv[k][j]; } }
;     __syncthreads();
;     const int lane = F.lane; const int gw = F.bx * NWAVES + F.wave, NGW = F.G * NWAVES;
;     LAS int* asg_e = (LAS int*)(F.lds + LDSX_OFF); LAS int* asg_d = asg_e + 128; LAS float* asg_g = (LAS float*)(asg_e + 256); LAS int* wgcnt = asg_e + 384; LAS int* wgbase = asg_e + 400;
;     int* ldst = (int*)(F.ws + WS_LIST + (size_t)l * 2 * MiB); float* lgate = (float*)(F.ws + WS_LIST + (size_t)l * 2 * MiB + MiB);
;     const int niter = (T + NGW - 1) / NGW;
;     for (int it = 0; it < niter; it += 2) {
;         const int rowA = gw + it * NGW, rowB = gw + (it + 1) * NGW; const int slot = it & 7;
;         const bool okA = rowA < T, okB = (it + 1 < niter) && rowB < T; const int rA = okA ? rowA : 0, rB = okB ? rowB : rA;
	ds_write2st64_b32 v0, v38, v39 offset1:32
	ds_write2st64_b32 v0, v40, v41 offset0:64 offset1:96
	v_add_u32_e32 v0, 0xe00, v66
	v_and_b32_e32 v0, -4, v0
	v_add3_u32 v0, 0, v0, v67
	s_waitcnt vmcnt(8)
	ds_write2st64_b32 v0, v62, v63 offset1:32
	ds_write2st64_b32 v0, v64, v65 offset0:64 offset1:96
	v_add_u32_e32 v0, 0x1000, v66
	v_and_b32_e32 v0, -4, v0
	v_add3_u32 v0, 0, v0, v67
	s_waitcnt vmcnt(7)
	ds_write2st64_b32 v0, v58, v59 offset1:32
	ds_write2st64_b32 v0, v60, v61 offset0:64 offset1:96
	v_add_u32_e32 v0, 0x1200, v66
	v_and_b32_e32 v0, -4, v0
	v_add3_u32 v0, 0, v0, v67
	s_waitcnt vmcnt(6)
	ds_write2st64_b32 v0, v54, v55 offset1:32
	ds_write2st64_b32 v0, v56, v57 offset0:64 offset1:96
	v_add_u32_e32 v0, 0x1400, v66
	v_and_b32_e32 v0, -4, v0
	v_add3_u32 v0, 0, v0, v67
	s_waitcnt vmcnt(5)
	ds_write2st64_b32 v0, v50, v51 offset1:32
	ds_write2st64_b32 v0, v52, v53 offset0:64 offset1:96
	v_add_u32_e32 v0, 0x1600, v66
	v_and_b32_e32 v0, -4, v0
	v_add3_u32 v0, 0, v0, v67
	s_waitcnt vmcnt(4)
	ds_write2st64_b32 v0, v46, v47 offset1:32
	ds_write2st64_b32 v0, v48, v49 offset0:64 offset1:96
	v_add_u32_e32 v0, 0x1800, v66
	v_and_b32_e32 v0, -4, v0
	v_add3_u32 v0, 0, v0, v67
	s_waitcnt vmcnt(3)
	ds_write2st64_b32 v0, v42, v43 offset1:32
	ds_write2st64_b32 v0, v44, v45 offset0:64 offset1:96
	v_add_u32_e32 v0, 0x1a00, v66
	v_and_b32_e32 v0, -4, v0
	v_add3_u32 v0, 0, v0, v67
	s_waitcnt vmcnt(2)
	ds_write2st64_b32 v0, v34, v35 offset1:32
	ds_write2st64_b32 v0, v36, v37 offset0:64 offset1:96
	v_add_u32_e32 v0, 0x1c00, v66
	v_and_b32_e32 v0, -4, v0
	v_add3_u32 v0, 0, v0, v67
	s_waitcnt vmcnt(1)
	ds_write2st64_b32 v0, v30, v31 offset1:32
	ds_write2st64_b32 v0, v32, v33 offset0:64 offset1:96
	v_add_u32_e32 v0, 0x1e00, v66
	v_and_b32_e32 v0, -4, v0
	v_add3_u32 v0, 0, v0, v67
	s_andn2_b64 vcc, exec, s[0:1]
	s_waitcnt vmcnt(0)
	ds_write2st64_b32 v0, v26, v27 offset1:32
	ds_write2st64_b32 v0, v28, v29 offset0:64 offset1:96
	s_waitcnt lgkmcnt(0)
	s_barrier
	s_cbranch_vccnz .LBB0_939
	v_and_b32_e32 v116, 63, v66
	v_lshlrev_b32_e32 v0, 4, v116
	v_lshl_add_u64 v[2:3], s[62:63], 0, v[0:1]
	v_and_b32_e32 v0, 64, v228
	v_add_u32_e32 v0, 64, v0
	v_xor_b32_e32 v4, 1, v228
	v_cmp_lt_i32_e32 vcc, v4, v0
	v_readlane_b32 s0, v246, 8
	v_readlane_b32 s1, v246, 9
	v_cndmask_b32_e32 v4, v228, v4, vcc
	v_lshlrev_b32_e32 v117, 2, v4
	v_xor_b32_e32 v4, 2, v228
	v_cmp_lt_i32_e32 vcc, v4, v0
	s_lshl_b32 s88, s0, 1
	s_ashr_i32 s16, s11, 6
	v_cndmask_b32_e32 v4, v228, v4, vcc
	v_lshlrev_b32_e32 v118, 2, v4
	v_xor_b32_e32 v4, 4, v228
	v_readlane_b32 s9, v247, 25
	v_cmp_lt_i32_e32 vcc, v4, v0
	s_mov_b32 s12, s0
	s_lshl_b64 s[0:1], s[88:89], 20
	s_add_i32 s68, s16, s9
	v_cndmask_b32_e32 v4, v228, v4, vcc
	s_add_u32 s0, s62, s0
	v_lshlrev_b32_e32 v119, 2, v4
	v_xor_b32_e32 v4, 8, v228
	s_addc_u32 s1, s63, s1
	v_cmp_lt_i32_e32 vcc, v4, v0
	s_add_u32 s64, s0, 0x100000
	s_addc_u32 s65, s1, 0
	v_cndmask_b32_e32 v4, v228, v4, vcc
	v_lshlrev_b32_e32 v120, 2, v4
	v_xor_b32_e32 v4, 16, v228
	s_add_u32 s66, s0, 0x200000
	v_cmp_lt_i32_e32 vcc, v4, v0
	s_addc_u32 s67, s1, 0
	s_lshl_b32 s0, s12, 6
	s_lshl_b64 s[12:13], s[88:89], 13
	v_cndmask_b32_e32 v4, v228, v4, vcc
	s_add_u32 s8, s8, s12
	v_lshlrev_b32_e32 v121, 2, v4
	v_xor_b32_e32 v4, 32, v228
	s_addc_u32 s9, s10, s13
	v_cmp_lt_i32_e32 vcc, v4, v0
	s_add_u32 s2, s2, s12
	s_addc_u32 s3, s3, s13
	v_cndmask_b32_e32 v0, v228, v4, vcc
	v_lshlrev_b32_e32 v122, 2, v0
	v_lshlrev_b32_e32 v0, 5, v116
	v_lshl_add_u64 v[8:9], s[8:9], 0, v[0:1]
	v_lshl_add_u64 v[10:11], s[2:3], 0, v[0:1]
	s_mov_b64 s[2:3], 0x1000
	v_lshl_add_u64 v[12:13], v[8:9], 0, s[2:3]
	v_lshl_add_u64 v[14:15], v[10:11], 0, s[2:3]
	s_mov_b64 s[2:3], 0x1800
	v_lshl_add_u64 v[16:17], v[8:9], 0, s[2:3]
	v_lshl_add_u64 v[18:19], v[10:11], 0, s[2:3]
	s_mov_b64 s[2:3], 0x6a800000
	v_lshl_add_u64 v[20:21], v[2:3], 0, s[2:3]
	s_mov_b64 s[2:3], 0x62800000
	s_mov_b32 s1, s89
	v_lshl_add_u64 v[22:23], v[2:3], 0, s[2:3]
	s_movk_i32 s2, 0x80
	v_cmp_gt_i32_e64 s[44:45], s2, v66
	s_add_i32 s2, 0, 0x20000
	s_lshl_b64 s[0:1], s[0:1], 2
	s_mov_b64 s[10:11], 0x5a800000
	s_add_u32 s0, s62, s0
	v_lshl_add_u64 v[6:7], v[2:3], 0, s[10:11]
	v_lshlrev_b32_e32 v2, 2, v228
	s_addc_u32 s1, s63, s1
	v_ashrrev_i32_e32 v67, 31, v66
	v_and_b32_e32 v123, 0x100, v2
	v_lshl_add_u64 v[2:3], v[66:67], 2, s[0:1]
	s_mov_b64 s[0:1], 0x8000
	v_lshl_add_u64 v[24:25], v[2:3], 0, s[0:1]
	v_readlane_b32 s0, v247, 46
	v_lshl_add_u32 v140, s16, 4, v116
	v_add_u32_e32 v139, s2, v68
	v_add_u32_e32 v142, s0, v68
	v_readlane_b32 s0, v247, 47
	v_add_u32_e32 v4, 2, v140
	v_readlane_b32 s2, v247, 45
	v_add_u32_e32 v143, s0, v68
	v_readlane_b32 s0, v247, 48
	s_mov_b32 s69, 0
	v_add_u32_e32 v0, 0, v0
	v_or_b32_e32 v124, 4, v123
	v_or_b32_e32 v125, 8, v123
	v_or_b32_e32 v126, 12, v123
	v_or_b32_e32 v127, 16, v123
	v_or_b32_e32 v128, 20, v123
	v_or_b32_e32 v129, 24, v123
	v_or_b32_e32 v130, 28, v123
	v_or_b32_e32 v131, 32, v123
	v_or_b32_e32 v132, 36, v123
	v_or_b32_e32 v133, 40, v123
	v_or_b32_e32 v134, 44, v123
	v_or_b32_e32 v135, 48, v123
	v_or_b32_e32 v136, 52, v123
	v_or_b32_e32 v137, 56, v123
	v_or_b32_e32 v138, 60, v123
	v_cmp_gt_u32_e64 s[40:41], 2, v116
	v_cmp_eq_u32_e64 s[42:43], 0, v116
	v_cmp_gt_i32_e64 s[46:47], 16, v66
	v_add_u32_e32 v141, s2, v68
	v_add_u32_e32 v144, s0, v68
	v_lshlrev_b32_e32 v145, 13, v116
	v_lshlrev_b32_e32 v146, 2, v4
	s_branch .LBB0_800

; #define GAS __attribute__((address_space(1)))
; __device__ __forceinline__ void unpack8h(const u32x4 w, float (&o)[8]) { o[0] = hlo(w.x); o[1] = hhi(w.x); o[2] = hlo(w.y); o[3] = hhi(w.y); o[4] = hlo(w.z); o[5] = hhi(w.z); o[6] = hlo(w.w); o[7] = hhi(w.w); }
; __device__ __forceinline__ void ln_rows(float (&v)[4][8], const float* g, const float* bta, int lane) {
;     float s = 0.f;
; #pragma unroll
;     for (int j = 0; j < 4; ++j)
; #pragma unroll
;         for (int e = 0; e < 8; ++e) s += v[j][e];
;     const float mean = wave_sum(s) * (1.f / DM); float q = 0.f;
; __device__ __forceinline__ void ln1_router_phase(const Args& a, Frame& F, int l) {
;     ...
;         const int rowA = gw + it * NGW, rowB = gw + (it + 1) * NGW; const int slot = it & 7;
;         const bool okA = rowA < T, okB = (it + 1 < niter) && rowB < T; const int rA = okA ? rowA : 0, rB = okB ? rowB : rA;
;         if (slot == 0) { if (F.tid < 128) asg_e[F.tid] = -1; __syncthreads(); }
;         float va[4][8], vb[4][8];
; #pragma unroll
;         for (int j = 0; j < 4; ++j) { unpack8h(*(const GAS u32x4*)(PRE + (size_t)rA * DM + 8 * lane + 512 * j), va[j]); unpack8h(*(const GAS u32x4*)(PRE + (size_t)rB * DM + 8 * lane + 512 * j), vb[j]); }
;         ln_rows(va, g, bta, lane); ln_rows(vb, g, bta, lane);
.LBB0_804:
	v_readlane_b32 s0, v247, 62
	s_mul_i32 s38, s69, s0
	v_readlane_b32 s1, v247, 63
	s_mov_b32 s2, s0
	s_add_i32 s38, s38, s68
	s_or_b32 s0, s69, 1
	s_add_i32 s71, s38, s2
	v_readlane_b32 s1, v246, 6
	s_cmp_lt_i32 s0, s1
	s_cselect_b64 s[0:1], -1, 0
	s_cmpk_lt_i32 s71, 0x4000
	s_cselect_b64 s[2:3], -1, 0
	s_and_b64 s[12:13], s[0:1], s[2:3]
	s_cmpk_lt_i32 s38, 0x4000
	s_cselect_b64 s[2:3], -1, 0
	s_and_b64 s[0:1], s[2:3], exec
	s_cselect_b32 s0, s38, 0
	s_and_b64 s[8:9], s[12:13], exec
	s_cselect_b32 s8, s71, s0
	s_ashr_i32 s1, s0, 31
	s_lshl_b64 s[50:51], s[0:1], 12
	s_ashr_i32 s9, s8, 31
	v_lshl_add_u64 v[2:3], v[6:7], 0, s[50:51]
	s_lshl_b64 s[10:11], s[8:9], 12
	global_load_dwordx4 v[36:39], v[2:3], off offset:3072
	global_load_dwordx4 v[48:51], v[2:3], off offset:2048
	global_load_dwordx4 v[62:65], v[2:3], off offset:1024
	global_load_dwordx4 v[66:69], v[2:3], off
	v_lshl_add_u64 v[2:3], v[6:7], 0, s[10:11]
	global_load_dwordx4 v[70:73], v[2:3], off offset:3072
	global_load_dwordx4 v[74:77], v[2:3], off offset:2048
	global_load_dwordx4 v[78:81], v[2:3], off offset:1024
	global_load_dwordx4 v[82:85], v[2:3], off
	s_mov_b32 s0, 0x3a000000
	s_mov_b32 s8, 0xf800000
	s_cmpk_gt_i32 s38, 0x3fff
	s_waitcnt vmcnt(0)
	v_cvt_f32_f16_sdwa v30, v37 dst_sel:DWORD dst_unused:UNUSED_PAD src0_sel:WORD_1
	v_cvt_f32_f16_e32 v32, v37
	s_waitcnt vmcnt(3)
	v_cvt_f32_f16_e32 v31, v71
	v_cvt_f32_f16_sdwa v54, v66 dst_sel:DWORD dst_unused:UNUSED_PAD src0_sel:WORD_1
	v_cvt_f32_f16_e32 v66, v66
	s_waitcnt vmcnt(0)
	v_cvt_f32_f16_e32 v55, v82
	v_cvt_f32_f16_sdwa v86, v67 dst_sel:DWORD dst_unused:UNUSED_PAD src0_sel:WORD_1
	v_cvt_f32_f16_e32 v88, v67
	v_cvt_f32_f16_sdwa v67, v82 dst_sel:DWORD dst_unused:UNUSED_PAD src0_sel:WORD_1
	v_cvt_f32_f16_e32 v87, v83
	v_cvt_f32_f16_sdwa v89, v83 dst_sel:DWORD dst_unused:UNUSED_PAD src0_sel:WORD_1
	v_cvt_f32_f16_sdwa v90, v68 dst_sel:DWORD dst_unused:UNUSED_PAD src0_sel:WORD_1
	v_cvt_f32_f16_e32 v68, v68
	v_cvt_f32_f16_sdwa v33, v71 dst_sel:DWORD dst_unused:UNUSED_PAD src0_sel:WORD_1
	v_cvt_f32_f16_e32 v35, v70
	v_cvt_f32_f16_sdwa v37, v70 dst_sel:DWORD dst_unused:UNUSED_PAD src0_sel:WORD_1
	v_cvt_f32_f16_e32 v91, v84
	v_mov_b32_e32 v70, v66
	v_mov_b32_e32 v71, v55
	v_cvt_f32_f16_sdwa v96, v69 dst_sel:DWORD dst_unused:UNUSED_PAD src0_sel:WORD_1
	v_cvt_f32_f16_e32 v98, v69
	v_cvt_f32_f16_sdwa v3, v73 dst_sel:DWORD dst_unused:UNUSED_PAD src0_sel:WORD_1
	v_cvt_f32_f16_e32 v4, v73
	v_cvt_f32_f16_e32 v26, v72
	v_cvt_f32_f16_sdwa v29, v72 dst_sel:DWORD dst_unused:UNUSED_PAD src0_sel:WORD_1
	v_cvt_f32_f16_sdwa v69, v84 dst_sel:DWORD dst_unused:UNUSED_PAD src0_sel:WORD_1
	v_mov_b32_e32 v72, v54
	v_mov_b32_e32 v73, v67
	v_pk_add_f32 v[70:71], v[70:71], 0 op_sel_hi:[1,0]
	v_cvt_f32_f16_sdwa v46, v48 dst_sel:DWORD dst_unused:UNUSED_PAD src0_sel:WORD_1
	v_cvt_f32_f16_e32 v52, v48
	v_cvt_f32_f16_sdwa v48, v49 dst_sel:DWORD dst_unused:UNUSED_PAD src0_sel:WORD_1
	v_cvt_f32_f16_e32 v60, v49
	v_cvt_f32_f16_e32 v47, v74
	v_cvt_f32_f16_sdwa v53, v74 dst_sel:DWORD dst_unused:UNUSED_PAD src0_sel:WORD_1
	v_cvt_f32_f16_e32 v49, v75
	v_cvt_f32_f16_sdwa v61, v75 dst_sel:DWORD dst_unused:UNUSED_PAD src0_sel:WORD_1
	v_cvt_f32_f16_e32 v97, v85
	v_mov_b32_e32 v74, v88
	v_mov_b32_e32 v75, v87
	v_pk_add_f32 v[70:71], v[70:71], v[72:73]
	v_cvt_f32_f16_sdwa v27, v38 dst_sel:DWORD dst_unused:UNUSED_PAD src0_sel:WORD_1
	v_cvt_f32_f16_e32 v28, v38
	v_cvt_f32_f16_e32 v38, v77
	v_cvt_f32_f16_sdwa v41, v77 dst_sel:DWORD dst_unused:UNUSED_PAD src0_sel:WORD_1
	v_cvt_f32_f16_e32 v43, v76
	v_cvt_f32_f16_sdwa v45, v76 dst_sel:DWORD dst_unused:UNUSED_PAD src0_sel:WORD_1
	v_cvt_f32_f16_sdwa v99, v85 dst_sel:DWORD dst_unused:UNUSED_PAD src0_sel:WORD_1
	v_mov_b32_e32 v76, v86
	v_pk_add_f32 v[70:71], v[70:71], v[74:75]
	v_mov_b32_e32 v77, v89
	v_cvt_f32_f16_e32 v2, v39
	v_cvt_f32_f16_sdwa v5, v39 dst_sel:DWORD dst_unused:UNUSED_PAD src0_sel:WORD_1
	v_cvt_f32_f16_sdwa v39, v51 dst_sel:DWORD dst_unused:UNUSED_PAD src0_sel:WORD_1
	v_cvt_f32_f16_e32 v40, v51
	v_cvt_f32_f16_e32 v58, v62
	v_cvt_f32_f16_e32 v51, v78
	v_pk_add_f32 v[70:71], v[70:71], v[76:77]
	v_mov_b32_e32 v72, v68
	v_mov_b32_e32 v73, v91
	v_cvt_f32_f16_sdwa v42, v50 dst_sel:DWORD dst_unused:UNUSED_PAD src0_sel:WORD_1
	v_cvt_f32_f16_e32 v44, v50
	v_cvt_f32_f16_sdwa v50, v62 dst_sel:DWORD dst_unused:UNUSED_PAD src0_sel:WORD_1
	v_cvt_f32_f16_sdwa v59, v78 dst_sel:DWORD dst_unused:UNUSED_PAD src0_sel:WORD_1
	v_pk_add_f32 v[70:71], v[70:71], v[72:73]
	v_mov_b32_e32 v72, v90
	v_mov_b32_e32 v73, v69
	v_cvt_f32_f16_e32 v62, v63
	v_cvt_f32_f16_e32 v57, v79
	v_pk_add_f32 v[70:71], v[70:71], v[72:73]
	v_mov_b32_e32 v72, v98
	v_mov_b32_e32 v73, v97
	v_cvt_f32_f16_sdwa v56, v63 dst_sel:DWORD dst_unused:UNUSED_PAD src0_sel:WORD_1
	v_cvt_f32_f16_sdwa v63, v79 dst_sel:DWORD dst_unused:UNUSED_PAD src0_sel:WORD_1
	v_pk_add_f32 v[70:71], v[70:71], v[72:73]
	v_mov_b32_e32 v72, v96
	v_mov_b32_e32 v73, v99
	v_cvt_f32_f16_sdwa v92, v64 dst_sel:DWORD dst_unused:UNUSED_PAD src0_sel:WORD_1
	v_cvt_f32_f16_e32 v64, v64
	v_cvt_f32_f16_e32 v93, v80
	v_pk_add_f32 v[70:71], v[70:71], v[72:73]
	v_mov_b32_e32 v72, v58
	v_mov_b32_e32 v73, v51
	v_cvt_f32_f16_sdwa v94, v65 dst_sel:DWORD dst_unused:UNUSED_PAD src0_sel:WORD_1
	v_cvt_f32_f16_e32 v102, v65
	v_cvt_f32_f16_sdwa v65, v80 dst_sel:DWORD dst_unused:UNUSED_PAD src0_sel:WORD_1
	v_pk_add_f32 v[70:71], v[70:71], v[72:73]
	v_mov_b32_e32 v72, v50
	v_mov_b32_e32 v73, v59
	v_cvt_f32_f16_e32 v95, v81
	v_pk_add_f32 v[70:71], v[70:71], v[72:73]
	v_mov_b32_e32 v72, v62
	v_mov_b32_e32 v73, v57
	v_cvt_f32_f16_sdwa v103, v81 dst_sel:DWORD dst_unused:UNUSED_PAD src0_sel:WORD_1
; __device__ __forceinline__ void ln_rows(float (&v)[4][8], const float* g, const float* bta, int lane) {
;     ...
;     const float mean = wave_sum(s) * (1.f / DM); float q = 0.f;
; #pragma unroll
;     for (int j = 0; j < 4; ++j)
; #pragma unroll
;         for (int e = 0; e < 8; ++e) { v[j][e] -= mean; q += v[j][e] * v[j][e]; }
;     const float rstd = 1.0f / sqrtf(wave_sum(q) * (1.f / DM) + LN_EPS);
	v_pk_add_f32 v[70:71], v[70:71], v[72:73]
	v_mov_b32_e32 v72, v56
	v_mov_b32_e32 v73, v63
	v_pk_add_f32 v[70:71], v[70:71], v[72:73]
	v_mov_b32_e32 v72, v64
	v_mov_b32_e32 v73, v93
	v_pk_add_f32 v[70:71], v[70:71], v[72:73]
	v_mov_b32_e32 v72, v92
	v_mov_b32_e32 v73, v65
	v_pk_add_f32 v[70:71], v[70:71], v[72:73]
	v_mov_b32_e32 v72, v102
	v_mov_b32_e32 v73, v95
	v_pk_add_f32 v[70:71], v[70:71], v[72:73]
	v_mov_b32_e32 v72, v94
	v_mov_b32_e32 v73, v103
	v_pk_add_f32 v[70:71], v[70:71], v[72:73]
	v_mov_b32_e32 v72, v52
	v_mov_b32_e32 v73, v47
	v_pk_add_f32 v[70:71], v[70:71], v[72:73]
	v_mov_b32_e32 v72, v46
	v_mov_b32_e32 v73, v53
	v_pk_add_f32 v[70:71], v[70:71], v[72:73]
	v_mov_b32_e32 v72, v60
	v_mov_b32_e32 v73, v49
	v_pk_add_f32 v[70:71], v[70:71], v[72:73]
	v_mov_b32_e32 v72, v48
	v_mov_b32_e32 v73, v61
	v_cvt_f32_f16_sdwa v34, v36 dst_sel:DWORD dst_unused:UNUSED_PAD src0_sel:WORD_1
	v_cvt_f32_f16_e32 v36, v36
	v_pk_add_f32 v[70:71], v[70:71], v[72:73]
	v_mov_b32_e32 v72, v44
	v_mov_b32_e32 v73, v43
	v_pk_add_f32 v[70:71], v[70:71], v[72:73]
	v_mov_b32_e32 v72, v42
	v_mov_b32_e32 v73, v45
	v_pk_add_f32 v[70:71], v[70:71], v[72:73]
	v_mov_b32_e32 v72, v40
	v_mov_b32_e32 v73, v38
	v_pk_add_f32 v[70:71], v[70:71], v[72:73]
	v_mov_b32_e32 v72, v39
	v_mov_b32_e32 v73, v41
	v_pk_add_f32 v[70:71], v[70:71], v[72:73]
	v_mov_b32_e32 v72, v36
	v_mov_b32_e32 v73, v35
	v_pk_add_f32 v[70:71], v[70:71], v[72:73]
	v_mov_b32_e32 v72, v34
	v_mov_b32_e32 v73, v37
	v_pk_add_f32 v[70:71], v[70:71], v[72:73]
	v_mov_b32_e32 v72, v32
	v_mov_b32_e32 v73, v31
	v_pk_add_f32 v[70:71], v[70:71], v[72:73]
	v_mov_b32_e32 v72, v30
	v_mov_b32_e32 v73, v33
	v_pk_add_f32 v[70:71], v[70:71], v[72:73]
	v_mov_b32_e32 v72, v28
	v_mov_b32_e32 v73, v26
	v_pk_add_f32 v[70:71], v[70:71], v[72:73]
	v_mov_b32_e32 v72, v27
	v_mov_b32_e32 v73, v29
	v_pk_add_f32 v[70:71], v[70:71], v[72:73]
	v_mov_b32_e32 v72, v2
	v_mov_b32_e32 v73, v4
	v_pk_add_f32 v[70:71], v[70:71], v[72:73]
	v_mov_b32_e32 v72, v5
	v_mov_b32_e32 v73, v3
	v_pk_add_f32 v[70:71], v[70:71], v[72:73]
	s_waitcnt lgkmcnt(0)
	s_nop 0
	v_add_f32_dpp v70, v70, v70 quad_perm:[1,0,3,2] row_mask:0xf bank_mask:0xf
	v_add_f32_dpp v71, v71, v71 quad_perm:[1,0,3,2] row_mask:0xf bank_mask:0xf
	s_waitcnt lgkmcnt(0)
	v_add_f32_dpp v70, v70, v70 quad_perm:[2,3,0,1] row_mask:0xf bank_mask:0xf
	v_add_f32_dpp v71, v71, v71 quad_perm:[2,3,0,1] row_mask:0xf bank_mask:0xf
	s_waitcnt lgkmcnt(0)
	v_add_f32_dpp v70, v70, v70 row_half_mirror row_mask:0xf bank_mask:0xf
	v_add_f32_dpp v71, v71, v71 row_half_mirror row_mask:0xf bank_mask:0xf
	s_waitcnt lgkmcnt(0)
	v_add_f32_dpp v70, v70, v70 row_mirror row_mask:0xf bank_mask:0xf
	v_add_f32_dpp v71, v71, v71 row_mirror row_mask:0xf bank_mask:0xf
	s_waitcnt lgkmcnt(0)
	v_mov_b32_e32 v72, v70
	v_mov_b32_e32 v73, v71
	s_nop 0
	v_permlane16_swap_b32_e32 v70, v72
	v_permlane16_swap_b32_e32 v71, v73
	v_pk_add_f32 v[70:71], v[70:71], v[72:73]
	s_waitcnt lgkmcnt(0)
	v_mov_b32_e32 v72, v70
	v_mov_b32_e32 v73, v71
	s_nop 0
	v_permlane32_swap_b32_e32 v70, v72
	v_permlane32_swap_b32_e32 v71, v73
	v_pk_add_f32 v[80:81], v[70:71], v[72:73]
	s_nop 0
	v_pk_fma_f32 v[112:113], v[80:81], s[0:1], v[54:55] op_sel_hi:[1,0,1] neg_lo:[1,0,0] neg_hi:[1,0,0]
	v_pk_fma_f32 v[100:101], v[80:81], s[0:1], v[66:67] op_sel_hi:[1,0,1] neg_lo:[1,0,0] neg_hi:[1,0,0]
	v_pk_mul_f32 v[54:55], v[112:113], v[112:113]
	v_pk_mul_f32 v[148:149], v[80:81], s[0:1] op_sel_hi:[1,0]
	v_pk_fma_f32 v[164:165], v[100:101], v[100:101], v[54:55]
	v_pk_fma_f32 v[54:55], v[80:81], s[0:1], v[88:89] op_sel_hi:[1,0,1] neg_lo:[1,0,0] neg_hi:[1,0,0]
	v_pk_fma_f32 v[104:105], v[80:81], s[0:1], v[86:87] op_sel_hi:[1,0,1] neg_lo:[1,0,0] neg_hi:[1,0,0]
	v_pk_mul_f32 v[166:167], v[54:55], v[54:55]
	v_pk_mul_f32 v[168:169], v[104:105], v[104:105]
	v_pk_fma_f32 v[110:111], v[80:81], s[0:1], v[68:69] op_sel_hi:[1,0,1] neg_lo:[1,0,0] neg_hi:[1,0,0]
	v_pk_fma_f32 v[114:115], v[80:81], s[0:1], v[90:91] op_sel_hi:[1,0,1] neg_lo:[1,0,0] neg_hi:[1,0,0]
	v_pk_fma_f32 v[88:89], v[80:81], s[0:1], v[98:99] op_sel_hi:[1,0,1] neg_lo:[1,0,0] neg_hi:[1,0,0]
	v_pk_fma_f32 v[106:107], v[80:81], s[0:1], v[96:97] op_sel_hi:[1,0,1] neg_lo:[1,0,0] neg_hi:[1,0,0]
	v_pk_fma_f32 v[86:87], v[80:81], s[0:1], v[58:59] op_sel_hi:[1,0,1] neg_lo:[1,0,0] neg_hi:[1,0,0]
	v_pk_fma_f32 v[96:97], v[80:81], s[0:1], v[50:51] op_sel_hi:[1,0,1] neg_lo:[1,0,0] neg_hi:[1,0,0]
	v_pk_fma_f32 v[50:51], v[80:81], s[0:1], v[62:63] op_sel_hi:[1,0,1] neg_lo:[1,0,0] neg_hi:[1,0,0]
	v_pk_fma_f32 v[90:91], v[80:81], s[0:1], v[56:57] op_sel_hi:[1,0,1] neg_lo:[1,0,0] neg_hi:[1,0,0]
	v_pk_fma_f32 v[98:99], v[80:81], s[0:1], v[64:65] op_sel_hi:[1,0,1] neg_lo:[1,0,0] neg_hi:[1,0,0]
	v_pk_fma_f32 v[108:109], v[80:81], s[0:1], v[92:93] op_sel_hi:[1,0,1] neg_lo:[1,0,0] neg_hi:[1,0,0]
	v_pk_fma_f32 v[56:57], v[80:81], s[0:1], v[102:103] op_sel_hi:[1,0,1] neg_lo:[1,0,0] neg_hi:[1,0,0]
	v_pk_fma_f32 v[102:103], v[80:81], s[0:1], v[94:95] op_sel_hi:[1,0,1] neg_lo:[1,0,0] neg_hi:[1,0,0]
	v_pk_fma_f32 v[58:59], v[80:81], s[0:1], v[52:53] op_sel_hi:[1,0,1] neg_lo:[1,0,0] neg_hi:[1,0,0]
	v_pk_fma_f32 v[92:93], v[80:81], s[0:1], v[46:47] op_sel_hi:[1,0,1] neg_lo:[1,0,0] neg_hi:[1,0,0]
	v_pk_fma_f32 v[66:67], v[80:81], s[0:1], v[60:61] op_sel_hi:[1,0,1] neg_lo:[1,0,0] neg_hi:[1,0,0]
	v_pk_fma_f32 v[62:63], v[80:81], s[0:1], v[48:49] op_sel_hi:[1,0,1] neg_lo:[1,0,0] neg_hi:[1,0,0]
	v_pk_fma_f32 v[60:61], v[80:81], s[0:1], v[44:45] op_sel_hi:[1,0,1] neg_lo:[1,0,0] neg_hi:[1,0,0]
	v_pk_fma_f32 v[94:95], v[80:81], s[0:1], v[42:43] op_sel_hi:[1,0,1] neg_lo:[1,0,0] neg_hi:[1,0,0]
; #define GAS __attribute__((address_space(1)))
; __device__ __forceinline__ void ln_rows(float (&v)[4][8], const float* g, const float* bta, int lane) {
;     ...
;     const float mean = wave_sum(s) * (1.f / DM); float q = 0.f;
; #pragma unroll
;     for (int j = 0; j < 4; ++j)
; #pragma unroll
;         for (int e = 0; e < 8; ++e) { v[j][e] -= mean; q += v[j][e] * v[j][e]; }
;     const float rstd = 1.0f / sqrtf(wave_sum(q) * (1.f / DM) + LN_EPS);
; #pragma unroll
;     for (int j = 0; j < 4; ++j) { const f32x4 g0 = *(const GAS f32x4*)(g + 8 * lane + 512 * j), g1 = *(const GAS f32x4*)(g + 8 * lane + 512 * j + 4), b0 = *(const GAS f32x4*)(bta + 8 * lane + 512 * j), b1 = *(const GAS f32x4*)(bta + 8 * lane + 512 * j + 4);
	v_pk_fma_f32 v[68:69], v[80:81], s[0:1], v[40:41] op_sel_hi:[1,0,1] neg_lo:[1,0,0] neg_hi:[1,0,0]
	v_pk_fma_f32 v[74:75], v[80:81], s[0:1], v[36:37] op_sel_hi:[1,0,1] neg_lo:[1,0,0] neg_hi:[1,0,0]
	v_pk_fma_f32 v[70:71], v[80:81], s[0:1], v[34:35] op_sel_hi:[1,0,1] neg_lo:[1,0,0] neg_hi:[1,0,0]
	v_pk_fma_f32 v[82:83], v[80:81], s[0:1], v[32:33] op_sel_hi:[1,0,1] neg_lo:[1,0,0] neg_hi:[1,0,0]
	v_pk_fma_f32 v[78:79], v[80:81], s[0:1], v[30:31] op_sel_hi:[1,0,1] neg_lo:[1,0,0] neg_hi:[1,0,0]
	v_pk_fma_f32 v[76:77], v[80:81], s[0:1], v[28:29] op_sel_hi:[1,0,1] neg_lo:[1,0,0] neg_hi:[1,0,0]
	v_pk_fma_f32 v[84:85], v[80:81], s[0:1], v[2:3] op_sel_hi:[1,0,1] neg_lo:[1,0,0] neg_hi:[1,0,0]
	v_pk_add_f32 v[80:81], v[4:5], v[148:149] op_sel:[0,1] op_sel_hi:[1,0] neg_lo:[0,1] neg_hi:[0,1]
	v_add_f32_e32 v4, v166, v164
	v_pk_mul_f32 v[170:171], v[110:111], v[110:111]
	v_add_f32_e32 v4, v168, v4
	v_pk_mul_f32 v[172:173], v[114:115], v[114:115]
	v_add_f32_e32 v4, v170, v4
	v_pk_mul_f32 v[174:175], v[88:89], v[88:89]
	v_add_f32_e32 v4, v172, v4
	v_pk_mul_f32 v[176:177], v[106:107], v[106:107]
	v_add_f32_e32 v4, v174, v4
	v_pk_mul_f32 v[178:179], v[86:87], v[86:87]
	v_add_f32_e32 v4, v176, v4
	v_pk_mul_f32 v[180:181], v[96:97], v[96:97]
	v_add_f32_e32 v4, v178, v4
	v_pk_mul_f32 v[182:183], v[50:51], v[50:51]
	v_add_f32_e32 v4, v180, v4
	v_pk_mul_f32 v[184:185], v[90:91], v[90:91]
	v_add_f32_e32 v4, v182, v4
	v_pk_mul_f32 v[186:187], v[98:99], v[98:99]
	v_add_f32_e32 v4, v184, v4
	v_pk_mul_f32 v[188:189], v[108:109], v[108:109]
	v_add_f32_e32 v4, v186, v4
	v_pk_mul_f32 v[190:191], v[56:57], v[56:57]
	v_add_f32_e32 v4, v188, v4
	v_pk_mul_f32 v[192:193], v[102:103], v[102:103]
	v_add_f32_e32 v4, v190, v4
	v_pk_mul_f32 v[52:53], v[58:59], v[58:59]
	v_add_f32_e32 v4, v192, v4
	v_pk_mul_f32 v[200:201], v[92:93], v[92:93]
	v_add_f32_e32 v4, v52, v4
	v_pk_mul_f32 v[202:203], v[66:67], v[66:67]
	v_add_f32_e32 v4, v200, v4
	v_pk_mul_f32 v[204:205], v[62:63], v[62:63]
	v_add_f32_e32 v4, v202, v4
	v_pk_mul_f32 v[206:207], v[60:61], v[60:61]
	v_add_f32_e32 v4, v204, v4
	v_pk_mul_f32 v[208:209], v[94:95], v[94:95]
	v_add_f32_e32 v4, v206, v4
	v_pk_mul_f32 v[210:211], v[68:69], v[68:69]
	v_pk_add_f32 v[64:65], v[38:39], v[148:149] op_sel:[0,1] op_sel_hi:[1,0] neg_lo:[0,1] neg_hi:[0,1]
	v_add_f32_e32 v4, v208, v4
	v_pk_mul_f32 v[212:213], v[64:65], v[64:65]
	v_add_f32_e32 v4, v210, v4
	v_pk_mul_f32 v[214:215], v[74:75], v[74:75]
	v_add_f32_e32 v4, v213, v4
	v_pk_mul_f32 v[216:217], v[70:71], v[70:71]
	v_add_f32_e32 v4, v214, v4
	v_pk_mul_f32 v[32:33], v[82:83], v[82:83]
	v_add_f32_e32 v4, v216, v4
	v_pk_mul_f32 v[30:31], v[78:79], v[78:79]
	v_add_f32_e32 v4, v32, v4
	v_pk_mul_f32 v[28:29], v[76:77], v[76:77]
	v_pk_add_f32 v[72:73], v[26:27], v[148:149] op_sel:[0,1] op_sel_hi:[1,0] neg_lo:[0,1] neg_hi:[0,1]
	v_add_f32_e32 v4, v30, v4
	v_pk_mul_f32 v[26:27], v[72:73], v[72:73]
	v_add_f32_e32 v4, v28, v4
	v_add_f32_e32 v4, v27, v4
	v_add_f32_e32 v27, v169, v165
	v_add_f32_e32 v27, v167, v27
	v_add_f32_e32 v27, v173, v27
	v_add_f32_e32 v27, v171, v27
	v_add_f32_e32 v27, v177, v27
	v_pk_mov_b32 v[2:3], v[80:81], v[84:85] op_sel:[1,0]
	v_add_f32_e32 v27, v175, v27
	v_pk_mul_f32 v[2:3], v[2:3], v[2:3]
	v_add_f32_e32 v27, v181, v27
	v_add_f32_e32 v3, v3, v4
	v_add_f32_e32 v27, v179, v27
	v_add_f32_e32 v2, v2, v3
	v_add_f32_e32 v27, v185, v27
	v_add_f32_e32 v27, v183, v27
	v_add_f32_e32 v27, v189, v27
	v_add_f32_e32 v27, v187, v27
	v_add_f32_e32 v27, v193, v27
	v_add_f32_e32 v27, v191, v27
	s_waitcnt lgkmcnt(0)
	v_add_f32_dpp v2, v2, v2 quad_perm:[1,0,3,2] row_mask:0xf bank_mask:0xf
	v_add_f32_e32 v27, v201, v27
	v_add_f32_e32 v27, v53, v27
	v_add_f32_e32 v27, v205, v27
	v_add_f32_e32 v27, v203, v27
	v_add_f32_e32 v27, v209, v27
	v_add_f32_e32 v27, v207, v27
	s_waitcnt lgkmcnt(0)
	v_add_f32_dpp v2, v2, v2 quad_perm:[2,3,0,1] row_mask:0xf bank_mask:0xf
	v_add_f32_e32 v27, v212, v27
	v_add_f32_e32 v27, v211, v27
	v_add_f32_e32 v27, v217, v27
	v_add_f32_e32 v27, v215, v27
	v_add_f32_e32 v27, v31, v27
	v_add_f32_e32 v27, v33, v27
	global_load_dwordx4 v[34:37], v[8:9], off offset:16
	global_load_dwordx4 v[38:41], v[8:9], off
	global_load_dwordx4 v[42:45], v[10:11], off offset:16
	global_load_dwordx4 v[46:49], v[10:11], off
	s_waitcnt lgkmcnt(0)
	v_add_f32_dpp v4, v2, v2 row_half_mirror row_mask:0xf bank_mask:0xf
	v_pk_mov_b32 v[2:3], v[84:85], v[80:81] op_sel:[1,0]
	v_add_f32_e32 v26, v26, v27
	v_pk_mul_f32 v[2:3], v[2:3], v[2:3]
	v_add_f32_e32 v26, v29, v26
	global_load_dwordx4 v[148:151], v[8:9], off offset:2064
	global_load_dwordx4 v[152:155], v[8:9], off offset:2048
	global_load_dwordx4 v[156:159], v[10:11], off offset:2064
	global_load_dwordx4 v[160:163], v[10:11], off offset:2048
	v_add_f32_e32 v3, v3, v26
	global_load_dwordx4 v[164:167], v[12:13], off
	global_load_dwordx4 v[168:171], v[12:13], off offset:16
	global_load_dwordx4 v[172:175], v[14:15], off
	global_load_dwordx4 v[176:179], v[14:15], off offset:16
	global_load_dwordx4 v[180:183], v[16:17], off
	global_load_dwordx4 v[184:187], v[16:17], off offset:16
	global_load_dwordx4 v[188:191], v[18:19], off
	global_load_dwordx4 v[200:203], v[18:19], off offset:16
	v_add_f32_e32 v2, v2, v3
	s_waitcnt lgkmcnt(1)
	s_nop 0
	v_add_f32_dpp v2, v2, v2 quad_perm:[1,0,3,2] row_mask:0xf bank_mask:0xf
	s_waitcnt lgkmcnt(1)
	v_add_f32_dpp v4, v4, v4 row_mirror row_mask:0xf bank_mask:0xf
	s_waitcnt lgkmcnt(1)
	v_add_f32_dpp v2, v2, v2 quad_perm:[2,3,0,1] row_mask:0xf bank_mask:0xf
	s_waitcnt lgkmcnt(1)
	v_mov_b32_e32 v5, v4
	s_nop 1
	v_permlane16_swap_b32_e32 v4, v5
	v_add_f32_e32 v4, v4, v5
	s_waitcnt lgkmcnt(1)
; #define GAS __attribute__((address_space(1)))
; __device__ __forceinline__ void ln_rows(float (&v)[4][8], const float* g, const float* bta, int lane) {
;     ...
;     const float rstd = 1.0f / sqrtf(wave_sum(q) * (1.f / DM) + LN_EPS);
; #pragma unroll
;     for (int j = 0; j < 4; ++j) { const f32x4 g0 = *(const GAS f32x4*)(g + 8 * lane + 512 * j), g1 = *(const GAS f32x4*)(g + 8 * lane + 512 * j + 4), b0 = *(const GAS f32x4*)(bta + 8 * lane + 512 * j), b1 = *(const GAS f32x4*)(bta + 8 * lane + 512 * j + 4);
; #pragma unroll
;         for (int e = 0; e < 4; ++e) { v[j][e] = v[j][e] * rstd * g0[e] + b0[e]; v[j][4 + e] = v[j][4 + e] * rstd * g1[e] + b1[e]; } }
	v_add_f32_dpp v2, v2, v2 row_half_mirror row_mask:0xf bank_mask:0xf
	s_waitcnt lgkmcnt(1)
	v_mov_b32_e32 v5, v4
	s_nop 1
	v_permlane32_swap_b32_e32 v4, v5
	v_add_f32_e32 v4, v4, v5
	v_fmamk_f32 v4, v4, 0x3a000000, v230
	v_mul_f32_e32 v5, 0x4f800000, v4
	v_cmp_gt_f32_e32 vcc, s8, v4
	s_waitcnt lgkmcnt(0)
	v_add_f32_dpp v2, v2, v2 row_mirror row_mask:0xf bank_mask:0xf
	v_cndmask_b32_e32 v4, v4, v5, vcc
	v_sqrt_f32_e32 v5, v4
	s_waitcnt lgkmcnt(0)
	v_mov_b32_e32 v3, v2
	s_nop 1
	v_permlane16_swap_b32_e32 v2, v3
	v_add_f32_e32 v2, v2, v3
	v_add_u32_e32 v26, -1, v5
	v_fma_f32 v27, -v26, v5, v4
	v_cmp_ge_f32_e64 s[0:1], 0, v27
	v_add_u32_e32 v27, 1, v5
	s_waitcnt lgkmcnt(0)
	v_mov_b32_e32 v3, v2
	s_nop 1
	v_permlane32_swap_b32_e32 v2, v3
	v_add_f32_e32 v2, v2, v3
	v_fmamk_f32 v2, v2, 0x3a000000, v230
	v_cndmask_b32_e64 v26, v5, v26, s[0:1]
	v_mul_f32_e32 v3, 0x4f800000, v2
	v_cmp_gt_f32_e64 s[0:1], s8, v2
	v_fma_f32 v5, -v27, v5, v4
	v_cmp_lt_f32_e64 s[48:49], 0, v5
	v_cndmask_b32_e64 v2, v2, v3, s[0:1]
	v_sqrt_f32_e32 v3, v2
	v_cndmask_b32_e64 v5, v26, v27, s[48:49]
	v_mul_f32_e32 v26, 0x37800000, v5
	v_cndmask_b32_e32 v5, v5, v26, vcc
	v_add_u32_e32 v27, -1, v3
	v_fma_f32 v28, -v27, v3, v2
	v_cmp_ge_f32_e64 s[48:49], 0, v28
	v_add_u32_e32 v28, 1, v3
	v_cmp_class_f32_e32 vcc, v4, v227
	v_cndmask_b32_e64 v27, v3, v27, s[48:49]
	v_fma_f32 v3, -v28, v3, v2
	v_cmp_lt_f32_e64 s[48:49], 0, v3
	v_cndmask_b32_e32 v4, v5, v4, vcc
	s_nop 0
	v_cndmask_b32_e64 v3, v27, v28, s[48:49]
	v_mul_f32_e32 v27, 0x37800000, v3
	v_cndmask_b32_e64 v3, v3, v27, s[0:1]
	v_cmp_class_f32_e64 s[0:1], v2, v227
	s_nop 1
	v_cndmask_b32_e64 v2, v3, v2, s[0:1]
	v_div_scale_f32 v3, s[0:1], v2, v2, 1.0
	v_rcp_f32_e32 v27, v3
	s_nop 0
	v_fma_f32 v5, -v3, v27, 1.0
	v_fmac_f32_e32 v27, v5, v27
	v_div_scale_f32 v5, vcc, 1.0, v2, 1.0
	v_mul_f32_e32 v26, v5, v27
	v_fma_f32 v28, -v3, v26, v5
	v_fmac_f32_e32 v26, v28, v27
	v_fma_f32 v3, -v3, v26, v5
	v_div_scale_f32 v5, s[0:1], v4, v4, 1.0
	v_rcp_f32_e32 v28, v5
	v_div_fmas_f32 v3, v3, v27, v26
	v_div_fixup_f32 v193, v3, v2, 1.0
	v_fma_f32 v2, -v5, v28, 1.0
	v_fmac_f32_e32 v28, v2, v28
	v_div_scale_f32 v2, vcc, 1.0, v4, 1.0
	v_mul_f32_e32 v3, v2, v28
	v_fma_f32 v26, -v5, v3, v2
	v_fmac_f32_e32 v3, v26, v28
	v_fma_f32 v2, -v5, v3, v2
	v_div_fmas_f32 v2, v2, v28, v3
	v_div_fixup_f32 v192, v2, v4, 1.0
	v_pk_mul_f32 v[2:3], v[112:113], v[192:193]
	v_pk_mul_f32 v[4:5], v[114:115], v[192:193]
	v_pk_mul_f32 v[26:27], v[100:101], v[192:193]
	v_pk_mul_f32 v[28:29], v[110:111], v[192:193]
	s_waitcnt vmcnt(12)
	v_pk_fma_f32 v[2:3], v[38:39], v[2:3], v[46:47] op_sel:[1,0,1] op_sel_hi:[0,1,0]
	v_pk_fma_f32 v[4:5], v[34:35], v[4:5], v[42:43] op_sel:[1,0,1] op_sel_hi:[0,1,0]
	v_pk_fma_f32 v[26:27], v[38:39], v[26:27], v[46:47]
	v_pk_fma_f32 v[28:29], v[34:35], v[28:29], v[42:43]
	v_pk_mul_f32 v[30:31], v[104:105], v[192:193]
	v_pk_mul_f32 v[32:33], v[106:107], v[192:193]
	v_pk_mul_f32 v[34:35], v[54:55], v[192:193]
	v_pk_mul_f32 v[38:39], v[88:89], v[192:193]
	v_pk_fma_f32 v[30:31], v[40:41], v[30:31], v[48:49] op_sel:[1,0,1] op_sel_hi:[0,1,0]
	v_pk_fma_f32 v[32:33], v[36:37], v[32:33], v[44:45] op_sel:[1,0,1] op_sel_hi:[0,1,0]
	v_pk_fma_f32 v[34:35], v[40:41], v[34:35], v[48:49]
	v_pk_fma_f32 v[36:37], v[36:37], v[38:39], v[44:45]
	v_pk_mul_f32 v[38:39], v[96:97], v[192:193]
	v_pk_mul_f32 v[40:41], v[108:109], v[192:193]
	v_pk_mul_f32 v[42:43], v[86:87], v[192:193]
	v_pk_mul_f32 v[44:45], v[98:99], v[192:193]
	v_pk_mul_f32 v[46:47], v[90:91], v[192:193]
	v_pk_mul_f32 v[48:49], v[102:103], v[192:193]
	v_pk_mul_f32 v[50:51], v[50:51], v[192:193]
	v_pk_mul_f32 v[52:53], v[56:57], v[192:193]
	v_pk_mul_f32 v[54:55], v[92:93], v[192:193]
	v_pk_mul_f32 v[56:57], v[94:95], v[192:193]
	v_pk_mul_f32 v[58:59], v[58:59], v[192:193]
	v_pk_mul_f32 v[60:61], v[60:61], v[192:193]
	v_pk_mul_f32 v[62:63], v[62:63], v[192:193]
	v_pk_mul_f32 v[64:65], v[64:65], v[192:193] op_sel:[0,1] op_sel_hi:[1,0]
	v_pk_mul_f32 v[66:67], v[66:67], v[192:193]
	v_pk_mul_f32 v[68:69], v[68:69], v[192:193]
	v_pk_mul_f32 v[70:71], v[70:71], v[192:193]
	v_pk_mul_f32 v[72:73], v[72:73], v[192:193] op_sel:[0,1] op_sel_hi:[1,0]
	v_pk_mul_f32 v[74:75], v[74:75], v[192:193]
	v_pk_mul_f32 v[76:77], v[76:77], v[192:193]
	v_pk_mul_f32 v[78:79], v[78:79], v[192:193]
	v_pk_mul_f32 v[80:81], v[80:81], v[192:193] op_sel:[0,1] op_sel_hi:[1,0]
	v_pk_mul_f32 v[82:83], v[82:83], v[192:193]
	v_pk_mul_f32 v[84:85], v[84:85], v[192:193]
	s_waitcnt vmcnt(8)
	v_pk_fma_f32 v[38:39], v[152:153], v[38:39], v[160:161] op_sel:[1,0,1] op_sel_hi:[0,1,0]
	v_pk_fma_f32 v[40:41], v[148:149], v[40:41], v[156:157] op_sel:[1,0,1] op_sel_hi:[0,1,0]
	v_pk_fma_f32 v[42:43], v[152:153], v[42:43], v[160:161]
	v_pk_fma_f32 v[44:45], v[148:149], v[44:45], v[156:157]
	v_pk_fma_f32 v[46:47], v[154:155], v[46:47], v[162:163] op_sel:[1,0,1] op_sel_hi:[0,1,0]
	v_pk_fma_f32 v[48:49], v[150:151], v[48:49], v[158:159] op_sel:[1,0,1] op_sel_hi:[0,1,0]
	v_pk_fma_f32 v[50:51], v[154:155], v[50:51], v[162:163]
	v_pk_fma_f32 v[52:53], v[150:151], v[52:53], v[158:159]
	s_waitcnt vmcnt(5)
	v_pk_fma_f32 v[54:55], v[164:165], v[54:55], v[172:173] op_sel:[1,0,1] op_sel_hi:[0,1,0]
	s_waitcnt vmcnt(4)
	v_pk_fma_f32 v[56:57], v[168:169], v[56:57], v[176:177] op_sel:[1,0,1] op_sel_hi:[0,1,0]
	v_pk_fma_f32 v[58:59], v[164:165], v[58:59], v[172:173]
	v_pk_fma_f32 v[60:61], v[168:169], v[60:61], v[176:177]
	v_pk_fma_f32 v[62:63], v[166:167], v[62:63], v[174:175] op_sel:[1,0,1] op_sel_hi:[0,1,0]
	v_pk_fma_f32 v[64:65], v[170:171], v[64:65], v[178:179]
	v_pk_fma_f32 v[66:67], v[166:167], v[66:67], v[174:175]
	v_pk_fma_f32 v[68:69], v[170:171], v[68:69], v[178:179]
	s_waitcnt vmcnt(1)
	v_pk_fma_f32 v[70:71], v[180:181], v[70:71], v[188:189] op_sel:[1,0,1] op_sel_hi:[0,1,0]
	s_waitcnt vmcnt(0)
	v_pk_fma_f32 v[72:73], v[184:185], v[72:73], v[200:201]
	v_pk_fma_f32 v[74:75], v[180:181], v[74:75], v[188:189]
	v_pk_fma_f32 v[76:77], v[184:185], v[76:77], v[200:201]
	v_pk_fma_f32 v[78:79], v[182:183], v[78:79], v[190:191] op_sel:[1,0,1] op_sel_hi:[0,1,0]
	v_pk_fma_f32 v[80:81], v[186:187], v[80:81], v[202:203]
	v_pk_fma_f32 v[82:83], v[182:183], v[82:83], v[190:191]
	v_pk_fma_f32 v[84:85], v[186:187], v[84:85], v[202:203]
	s_cbranch_scc1 .LBB0_806
; #define GAS __attribute__((address_space(1)))
; __device__ __forceinline__ u32x4 pack8h(const float (&o)[8]) { u32x4 w; w.x = pkh2(o[0], o[1]); w.y = pkh2(o[2], o[3]); w.z = pkh2(o[4], o[5]); w.w = pkh2(o[6], o[7]); return w; }
; __device__ __forceinline__ u32x4 pack8(const float (&o)[8]) { u32x4 w; w.x = pk2(o[0], o[1]); w.y = pk2(o[2], o[3]); w.z = pk2(o[4], o[5]); w.w = pk2(o[6], o[7]); return w; }
; __device__ __forceinline__ void ln1_router_phase(const Args& a, Frame& F, int l) {
;     ...
;         if (okA) {
; #pragma unroll
;             for (int j = 0; j < 4; ++j) { *(GAS u32x4*)(X1B + (size_t)rA * DM + 8 * lane + 512 * j) = pack8(va[j]); *(GAS u32x4*)(X1H + (size_t)rA * DM + 8 * lane + 512 * j) = pack8h(va[j]); } }
	v_lshl_add_u64 v[90:91], v[20:21], 0, s[50:51]
	v_cvt_pk_bf16_f32 v86, v26, v2
	v_cvt_pk_bf16_f32 v87, v34, v30
	v_cvt_pk_bf16_f32 v88, v28, v4
	v_cvt_pk_bf16_f32 v89, v36, v32
	v_lshl_add_u64 v[92:93], v[22:23], 0, s[50:51]
	global_store_dwordx4 v[90:91], v[86:89], off
	s_nop 1
	v_cvt_pk_f16_f32 v86, v26, v2
	v_cvt_pk_f16_f32 v87, v34, v30
	v_cvt_pk_f16_f32 v88, v28, v4
	v_cvt_pk_f16_f32 v89, v36, v32
	global_store_dwordx4 v[92:93], v[86:89], off
	s_nop 1
	v_cvt_pk_bf16_f32 v86, v42, v38
	v_cvt_pk_bf16_f32 v87, v50, v46
	v_cvt_pk_bf16_f32 v88, v44, v40
	v_cvt_pk_bf16_f32 v89, v52, v48
	global_store_dwordx4 v[90:91], v[86:89], off offset:1024
	s_nop 1
	v_cvt_pk_f16_f32 v86, v42, v38
	v_cvt_pk_f16_f32 v87, v50, v46
	v_cvt_pk_f16_f32 v88, v44, v40
	v_cvt_pk_f16_f32 v89, v52, v48
	global_store_dwordx4 v[92:93], v[86:89], off offset:1024
	s_nop 1
	v_cvt_pk_bf16_f32 v86, v58, v54
	v_cvt_pk_bf16_f32 v87, v66, v62
	v_cvt_pk_bf16_f32 v88, v60, v56
	v_cvt_pk_bf16_f32 v89, v68, v65
	global_store_dwordx4 v[90:91], v[86:89], off offset:2048
	s_nop 1
	v_cvt_pk_f16_f32 v86, v58, v54
	v_cvt_pk_f16_f32 v87, v66, v62
	v_cvt_pk_f16_f32 v88, v60, v56
	v_cvt_pk_f16_f32 v89, v68, v65
	global_store_dwordx4 v[92:93], v[86:89], off offset:2048
	s_nop 1
	v_cvt_pk_bf16_f32 v86, v74, v70
	v_cvt_pk_bf16_f32 v87, v82, v78
	v_cvt_pk_bf16_f32 v88, v76, v73
	v_cvt_pk_bf16_f32 v89, v84, v81
	global_store_dwordx4 v[90:91], v[86:89], off offset:3072
	s_nop 1
	v_cvt_pk_f16_f32 v86, v74, v70
	v_cvt_pk_f16_f32 v87, v82, v78
	v_cvt_pk_f16_f32 v88, v76, v73
	v_cvt_pk_f16_f32 v89, v84, v81
	global_store_dwordx4 v[92:93], v[86:89], off offset:3072

; #define LAS __attribute__((address_space(3)))
; __device__ __forceinline__ void ln1_router_phase(const Args& a, Frame& F, int l) {
;     ...
; #pragma unroll 1
;         for (int e = 0; e < 16; ++e) { float sA = 0.f, sB = 0.f;
; #pragma unroll
;             for (int j = 0; j < 4; ++j) { const f32x4 w0 = *(const LAS f32x4*)(wl + e * DM + 8 * lane + 512 * j), w1 = *(const LAS f32x4*)(wl + e * DM + 8 * lane + 512 * j + 4);
;                 sA += (va[j][0] * w0[0] + va[j][1] * w0[1]) + (va[j][2] * w0[2] + va[j][3] * w0[3]) + (va[j][4] * w1[0] + va[j][5] * w1[1]) + (va[j][6] * w1[2] + va[j][7] * w1[3]);
;                 sB += (vb[j][0] * w0[0] + vb[j][1] * w0[1]) + (vb[j][2] * w0[2] + vb[j][3] * w0[3]) + (vb[j][4] * w1[0] + vb[j][5] * w1[1]) + (vb[j][6] * w1[2] + vb[j][7] * w1[3]); }
;             sA = wave_sum(sA); sB = wave_sum(sB); lgA = (lane == e) ? sA : lgA; lgB = (lane == e) ? sB : lgB; }
.Lmy_rt_loop:
	v_cmp_eq_u32_e32 vcc, s0, v145
	s_addk_i32 s0, 0x2000
	v_add_u32_e32 v99, s0, v0
	ds_read_b128 v[180:183], v99
	ds_read_b128 v[184:187], v99 offset:16
	ds_read_b128 v[188:191], v99 offset:2048
	ds_read_b128 v[200:203], v99 offset:2064
	ds_read_b128 v[204:207], v99 offset:4096
	ds_read_b128 v[208:211], v99 offset:4112
	ds_read_b128 v[212:215], v99 offset:6144
	ds_read_b128 v[92:95], v99 offset:6160
	s_waitcnt lgkmcnt(8)
	v_pk_mul_f32 v[96:97], v[2:3], v[148:149] op_sel:[0,1] op_sel_hi:[1,0]
	s_nop 0
	v_pk_fma_f32 v[148:149], v[26:27], v[148:149], v[96:97]
	v_pk_mul_f32 v[96:97], v[30:31], v[150:151] op_sel:[0,1] op_sel_hi:[1,0]
	s_nop 0
	v_pk_fma_f32 v[150:151], v[34:35], v[150:151], v[96:97]
	s_nop 0
	v_pk_add_f32 v[148:149], v[148:149], v[150:151]
	v_pk_mul_f32 v[150:151], v[4:5], v[152:153] op_sel:[0,1] op_sel_hi:[1,0]
	s_nop 0
	v_pk_fma_f32 v[150:151], v[28:29], v[152:153], v[150:151]
	s_nop 0
	v_pk_add_f32 v[148:149], v[148:149], v[150:151]
	v_pk_mul_f32 v[150:151], v[32:33], v[154:155] op_sel:[0,1] op_sel_hi:[1,0]
	s_nop 0
	v_pk_fma_f32 v[150:151], v[36:37], v[154:155], v[150:151]
	s_nop 0
	v_pk_add_f32 v[100:101], v[150:151], v[148:149]
	s_nop 0
	v_pk_add_f32 v[100:101], v[100:101], 0 op_sel_hi:[1,0]
	v_pk_mul_f32 v[96:97], v[38:39], v[156:157] op_sel:[0,1] op_sel_hi:[1,0]
	s_nop 0
	v_pk_fma_f32 v[156:157], v[42:43], v[156:157], v[96:97]
	v_pk_mul_f32 v[96:97], v[46:47], v[158:159] op_sel:[0,1] op_sel_hi:[1,0]
	s_nop 0
	v_pk_fma_f32 v[158:159], v[50:51], v[158:159], v[96:97]
	s_nop 0
	v_pk_add_f32 v[156:157], v[156:157], v[158:159]
	v_pk_mul_f32 v[158:159], v[40:41], v[160:161] op_sel:[0,1] op_sel_hi:[1,0]
	s_nop 0
	v_pk_fma_f32 v[158:159], v[44:45], v[160:161], v[158:159]
	s_nop 0
	v_pk_add_f32 v[102:103], v[156:157], v[158:159]
	v_pk_mul_f32 v[156:157], v[48:49], v[162:163] op_sel:[0,1] op_sel_hi:[1,0]
	s_nop 0
	v_pk_fma_f32 v[104:105], v[52:53], v[162:163], v[156:157]
	s_nop 0
	v_pk_add_f32 v[102:103], v[104:105], v[102:103]
	v_pk_mul_f32 v[96:97], v[54:55], v[164:165] op_sel:[0,1] op_sel_hi:[1,0]
	s_nop 0
	v_pk_fma_f32 v[164:165], v[58:59], v[164:165], v[96:97]
	v_pk_mul_f32 v[96:97], v[62:63], v[166:167] op_sel:[0,1] op_sel_hi:[1,0]
	v_pk_mul_f32 v[108:109], v[68:69], v[170:171]
	v_pk_fma_f32 v[166:167], v[66:67], v[166:167], v[96:97]
	v_pk_fma_f32 v[170:171], v[64:65], v[170:171], v[108:109] op_sel:[0,0,1] op_sel_hi:[1,1,0]
	v_pk_add_f32 v[106:107], v[164:165], v[166:167]
	v_pk_mul_f32 v[164:165], v[56:57], v[168:169] op_sel:[0,1] op_sel_hi:[1,0]
	v_pk_add_f32 v[100:101], v[100:101], v[102:103]
	v_pk_fma_f32 v[168:169], v[60:61], v[168:169], v[164:165]
	s_nop 0
	v_pk_add_f32 v[168:169], v[106:107], v[168:169]
	v_pk_mul_f32 v[110:111], v[70:71], v[172:173] op_sel:[0,1] op_sel_hi:[1,0]
	s_nop 0
	v_pk_fma_f32 v[172:173], v[74:75], v[172:173], v[110:111]
	v_pk_mul_f32 v[110:111], v[78:79], v[174:175] op_sel:[0,1] op_sel_hi:[1,0]
	v_pk_add_f32 v[168:169], v[170:171], v[168:169] op_sel:[0,1] op_sel_hi:[1,0]
	v_pk_fma_f32 v[174:175], v[82:83], v[174:175], v[110:111]
	v_pk_mul_f32 v[110:111], v[76:77], v[176:177]
	v_pk_add_f32 v[172:173], v[172:173], v[174:175]
	v_pk_fma_f32 v[174:175], v[72:73], v[176:177], v[110:111] op_sel:[0,0,1] op_sel_hi:[1,1,0]
	v_pk_add_f32 v[168:169], v[100:101], v[168:169] op_sel:[1,0] op_sel_hi:[0,1]
	v_pk_add_f32 v[172:173], v[172:173], v[174:175] op_sel:[1,0] op_sel_hi:[0,1]
	v_pk_mul_f32 v[174:175], v[84:85], v[178:179]
	s_nop 0
	v_pk_fma_f32 v[174:175], v[80:81], v[178:179], v[174:175] op_sel:[0,0,1] op_sel_hi:[1,1,0]
	s_nop 0
	v_pk_add_f32 v[172:173], v[174:175], v[172:173]
	s_nop 0
	v_pk_add_f32 v[88:89], v[168:169], v[172:173]
	s_nop 1
	v_add_f32_dpp v88, v88, v88 quad_perm:[1,0,3,2] row_mask:0xf bank_mask:0xf
	v_add_f32_dpp v89, v89, v89 quad_perm:[1,0,3,2] row_mask:0xf bank_mask:0xf
	s_nop 0
	v_add_f32_dpp v88, v88, v88 quad_perm:[2,3,0,1] row_mask:0xf bank_mask:0xf
	v_add_f32_dpp v89, v89, v89 quad_perm:[2,3,0,1] row_mask:0xf bank_mask:0xf
	s_nop 0
	v_add_f32_dpp v88, v88, v88 row_half_mirror row_mask:0xf bank_mask:0xf
	v_add_f32_dpp v89, v89, v89 row_half_mirror row_mask:0xf bank_mask:0xf
	s_nop 0
	v_add_f32_dpp v88, v88, v88 row_mirror row_mask:0xf bank_mask:0xf
	v_add_f32_dpp v89, v89, v89 row_mirror row_mask:0xf bank_mask:0xf
	v_mov_b32_e32 v90, v88
	v_mov_b32_e32 v91, v89
	s_nop 1
	v_permlane16_swap_b32_e32 v88, v90
	v_permlane16_swap_b32_e32 v89, v91
	v_add_f32_e32 v88, v88, v90
	v_add_f32_e32 v89, v89, v91
	v_mov_b32_e32 v90, v88
	v_mov_b32_e32 v91, v89
	s_nop 1
	v_permlane32_swap_b32_e32 v88, v90
	v_permlane32_swap_b32_e32 v89, v91
	v_add_f32_e32 v88, v88, v90
	v_add_f32_e32 v89, v89, v91
	v_cndmask_b32_e32 v86, v86, v88, vcc
	v_cndmask_b32_e32 v87, v87, v89, vcc
	v_cmp_eq_u32_e32 vcc, s0, v145
	s_addk_i32 s0, 0x2000
	v_add_u32_e32 v99, s0, v0
	ds_read_b128 v[148:151], v99
	ds_read_b128 v[152:155], v99 offset:16
	ds_read_b128 v[156:159], v99 offset:2048
	ds_read_b128 v[160:163], v99 offset:2064
	ds_read_b128 v[164:167], v99 offset:4096
	ds_read_b128 v[168:171], v99 offset:4112
	ds_read_b128 v[172:175], v99 offset:6144
	ds_read_b128 v[176:179], v99 offset:6160
	s_waitcnt lgkmcnt(8)
; #define LAS __attribute__((address_space(3)))
; __device__ __forceinline__ void ln1_router_phase(const Args& a, Frame& F, int l) {
;     ...
; #pragma unroll 1
;         for (int e = 0; e < 16; ++e) { float sA = 0.f, sB = 0.f;
; #pragma unroll
;             for (int j = 0; j < 4; ++j) { const f32x4 w0 = *(const LAS f32x4*)(wl + e * DM + 8 * lane + 512 * j), w1 = *(const LAS f32x4*)(wl + e * DM + 8 * lane + 512 * j + 4);
;                 sA += (va[j][0] * w0[0] + va[j][1] * w0[1]) + (va[j][2] * w0[2] + va[j][3] * w0[3]) + (va[j][4] * w1[0] + va[j][5] * w1[1]) + (va[j][6] * w1[2] + va[j][7] * w1[3]);
;                 sB += (vb[j][0] * w0[0] + vb[j][1] * w0[1]) + (vb[j][2] * w0[2] + vb[j][3] * w0[3]) + (vb[j][4] * w1[0] + vb[j][5] * w1[1]) + (vb[j][6] * w1[2] + vb[j][7] * w1[3]); }
;             sA = wave_sum(sA); sB = wave_sum(sB); lgA = (lane == e) ? sA : lgA; lgB = (lane == e) ? sB : lgB; }
	v_pk_mul_f32 v[96:97], v[2:3], v[180:181] op_sel:[0,1] op_sel_hi:[1,0]
	s_nop 0
	v_pk_fma_f32 v[180:181], v[26:27], v[180:181], v[96:97]
	v_pk_mul_f32 v[96:97], v[30:31], v[182:183] op_sel:[0,1] op_sel_hi:[1,0]
	s_nop 0
	v_pk_fma_f32 v[182:183], v[34:35], v[182:183], v[96:97]
	s_nop 0
	v_pk_add_f32 v[180:181], v[180:181], v[182:183]
	v_pk_mul_f32 v[182:183], v[4:5], v[184:185] op_sel:[0,1] op_sel_hi:[1,0]
	s_nop 0
	v_pk_fma_f32 v[182:183], v[28:29], v[184:185], v[182:183]
	s_nop 0
	v_pk_add_f32 v[180:181], v[180:181], v[182:183]
	v_pk_mul_f32 v[182:183], v[32:33], v[186:187] op_sel:[0,1] op_sel_hi:[1,0]
	s_nop 0
	v_pk_fma_f32 v[182:183], v[36:37], v[186:187], v[182:183]
	s_nop 0
	v_pk_add_f32 v[100:101], v[182:183], v[180:181]
	s_nop 0
	v_pk_add_f32 v[100:101], v[100:101], 0 op_sel_hi:[1,0]
	v_pk_mul_f32 v[96:97], v[38:39], v[188:189] op_sel:[0,1] op_sel_hi:[1,0]
	s_nop 0
	v_pk_fma_f32 v[188:189], v[42:43], v[188:189], v[96:97]
	v_pk_mul_f32 v[96:97], v[46:47], v[190:191] op_sel:[0,1] op_sel_hi:[1,0]
	s_nop 0
	v_pk_fma_f32 v[190:191], v[50:51], v[190:191], v[96:97]
	s_nop 0
	v_pk_add_f32 v[188:189], v[188:189], v[190:191]
	v_pk_mul_f32 v[190:191], v[40:41], v[200:201] op_sel:[0,1] op_sel_hi:[1,0]
	s_nop 0
	v_pk_fma_f32 v[190:191], v[44:45], v[200:201], v[190:191]
	s_nop 0
	v_pk_add_f32 v[102:103], v[188:189], v[190:191]
	v_pk_mul_f32 v[188:189], v[48:49], v[202:203] op_sel:[0,1] op_sel_hi:[1,0]
	s_nop 0
	v_pk_fma_f32 v[104:105], v[52:53], v[202:203], v[188:189]
	s_nop 0
	v_pk_add_f32 v[102:103], v[104:105], v[102:103]
	v_pk_mul_f32 v[96:97], v[54:55], v[204:205] op_sel:[0,1] op_sel_hi:[1,0]
	s_nop 0
	v_pk_fma_f32 v[204:205], v[58:59], v[204:205], v[96:97]
	v_pk_mul_f32 v[96:97], v[62:63], v[206:207] op_sel:[0,1] op_sel_hi:[1,0]
	v_pk_mul_f32 v[108:109], v[68:69], v[210:211]
	v_pk_fma_f32 v[206:207], v[66:67], v[206:207], v[96:97]
	v_pk_fma_f32 v[210:211], v[64:65], v[210:211], v[108:109] op_sel:[0,0,1] op_sel_hi:[1,1,0]
	v_pk_add_f32 v[106:107], v[204:205], v[206:207]
	v_pk_mul_f32 v[204:205], v[56:57], v[208:209] op_sel:[0,1] op_sel_hi:[1,0]
	v_pk_add_f32 v[100:101], v[100:101], v[102:103]
	v_pk_fma_f32 v[208:209], v[60:61], v[208:209], v[204:205]
	s_nop 0
	v_pk_add_f32 v[208:209], v[106:107], v[208:209]
	v_pk_mul_f32 v[110:111], v[70:71], v[212:213] op_sel:[0,1] op_sel_hi:[1,0]
	s_nop 0
	v_pk_fma_f32 v[212:213], v[74:75], v[212:213], v[110:111]
	v_pk_mul_f32 v[110:111], v[78:79], v[214:215] op_sel:[0,1] op_sel_hi:[1,0]
	v_pk_add_f32 v[208:209], v[210:211], v[208:209] op_sel:[0,1] op_sel_hi:[1,0]
	v_pk_fma_f32 v[214:215], v[82:83], v[214:215], v[110:111]
	v_pk_mul_f32 v[110:111], v[76:77], v[92:93]
	v_pk_add_f32 v[212:213], v[212:213], v[214:215]
	v_pk_fma_f32 v[214:215], v[72:73], v[92:93], v[110:111] op_sel:[0,0,1] op_sel_hi:[1,1,0]
	v_pk_add_f32 v[208:209], v[100:101], v[208:209] op_sel:[1,0] op_sel_hi:[0,1]
	v_pk_add_f32 v[212:213], v[212:213], v[214:215] op_sel:[1,0] op_sel_hi:[0,1]
	v_pk_mul_f32 v[214:215], v[84:85], v[94:95]
	s_nop 0
	v_pk_fma_f32 v[214:215], v[80:81], v[94:95], v[214:215] op_sel:[0,0,1] op_sel_hi:[1,1,0]
	s_nop 0
	v_pk_add_f32 v[212:213], v[214:215], v[212:213]
	s_nop 0
	v_pk_add_f32 v[88:89], v[208:209], v[212:213]
	s_nop 1
	v_add_f32_dpp v88, v88, v88 quad_perm:[1,0,3,2] row_mask:0xf bank_mask:0xf
	v_add_f32_dpp v89, v89, v89 quad_perm:[1,0,3,2] row_mask:0xf bank_mask:0xf
	s_nop 0
	v_add_f32_dpp v88, v88, v88 quad_perm:[2,3,0,1] row_mask:0xf bank_mask:0xf
	v_add_f32_dpp v89, v89, v89 quad_perm:[2,3,0,1] row_mask:0xf bank_mask:0xf
	s_nop 0
	v_add_f32_dpp v88, v88, v88 row_half_mirror row_mask:0xf bank_mask:0xf
	v_add_f32_dpp v89, v89, v89 row_half_mirror row_mask:0xf bank_mask:0xf
	s_nop 0
	v_add_f32_dpp v88, v88, v88 row_mirror row_mask:0xf bank_mask:0xf
	v_add_f32_dpp v89, v89, v89 row_mirror row_mask:0xf bank_mask:0xf
	v_mov_b32_e32 v90, v88
	v_mov_b32_e32 v91, v89
	s_nop 1
	v_permlane16_swap_b32_e32 v88, v90
	v_permlane16_swap_b32_e32 v89, v91
	v_add_f32_e32 v88, v88, v90
	v_add_f32_e32 v89, v89, v91
	v_mov_b32_e32 v90, v88
	v_mov_b32_e32 v91, v89
	s_nop 1
	v_permlane32_swap_b32_e32 v88, v90
	v_permlane32_swap_b32_e32 v89, v91
	v_add_f32_e32 v88, v88, v90
	v_add_f32_e32 v89, v89, v91
	v_cndmask_b32_e32 v86, v86, v88, vcc
	v_cndmask_b32_e32 v87, v87, v89, vcc
	s_cmp_lg_u32 s0, 0x20000
	s_cbranch_scc1 .Lmy_rt_loop
; #define LAS __attribute__((address_space(3)))
; __device__ __forceinline__ void route_row(float mylg, const float* br, int row, int ai0, int lane, LAS int* asg_e, LAS int* asg_d, LAS float* asg_g) {
;     const float myaff = 1.0f / (1.0f + expf(-mylg));
;     float aff[16], sel[16];
; #pragma unroll
;     for (int e = 0; e < 16; ++e) { aff[e] = __shfl(myaff, e); sel[e] = aff[e] + br[e]; }
;     float gs[4];
; #pragma unroll
;     for (int q = 0; q < 4; ++q) { const float s0 = sel[4 * q], s1 = sel[4 * q + 1], s2 = sel[4 * q + 2], s3 = sel[4 * q + 3];
;         gs[q] = fmaxf(fmaxf(fmaxf(s0 + s1, s0 + s2), fmaxf(s0 + s3, s1 + s2)), fmaxf(s1 + s3, s2 + s3)); }
;     int best = 0; float bs = gs[0];
; #pragma unroll
;     for (int q = 1; q < 4; ++q) if (gs[q] > bs) { bs = gs[q]; best = q; }
;     float cs[4], ca[4];
; #pragma unroll
;     for (int i = 0; i < 4; ++i) { cs[i] = best == 0 ? sel[i] : best == 1 ? sel[4 + i] : best == 2 ? sel[8 + i] : sel[12 + i]; ca[i] = best == 0 ? aff[i] : best == 1 ? aff[4 + i] : best == 2 ? aff[8 + i] : aff[12 + i]; }
	s_waitcnt lgkmcnt(0)
	s_andn2_b64 vcc, exec, s[2:3]
	s_cbranch_vccnz .LBB0_838
	v_mul_f32_e32 v2, 0xbfb8aa3b, v87
	v_rndne_f32_e32 v3, v2
	s_mov_b32 s0, 0xbfb8aa3b
	v_sub_f32_e32 v4, v2, v3
	v_fma_f32 v2, v87, s0, -v2
	v_fmac_f32_e32 v2, 0xb2a5705f, v87
	v_add_f32_e32 v2, v4, v2
	v_exp_f32_e32 v2, v2
	v_cvt_i32_f32_e32 v3, v3
	s_mov_b32 s0, 0x42ce8ed0
	v_cmp_nlt_f32_e32 vcc, s0, v87
	s_mov_b32 s0, 0xc2b17218
	v_ldexp_f32 v2, v2, v3
	v_cndmask_b32_e32 v2, 0, v2, vcc
	v_cmp_ngt_f32_e32 vcc, s0, v87
	v_mov_b64_e32 v[52:53], s[28:29]
	s_nop 0
	v_cndmask_b32_e32 v2, v231, v2, vcc
	v_add_f32_e32 v2, 1.0, v2
	v_div_scale_f32 v3, s[0:1], v2, v2, 1.0
	v_rcp_f32_e32 v4, v3
	s_nop 0
	v_fma_f32 v5, -v3, v4, 1.0
	v_fmac_f32_e32 v4, v5, v4
	v_div_scale_f32 v5, vcc, 1.0, v2, 1.0
	v_mul_f32_e32 v26, v5, v4
	v_fma_f32 v27, -v3, v26, v5
	v_fmac_f32_e32 v26, v27, v4
	v_fma_f32 v3, -v3, v26, v5
	v_div_fmas_f32 v3, v3, v4, v26
	v_div_fixup_f32 v56, v3, v2, 1.0
	v_mov_b32_e32 v2, v218
	v_mov_b32_e32 v3, v219
	v_mov_b32_e32 v4, v220
	v_mov_b32_e32 v5, v221
	ds_bpermute_b32 v28, v124, v56
	ds_bpermute_b32 v29, v126, v56
	ds_bpermute_b32 v34, v128, v56
	ds_bpermute_b32 v35, v130, v56
	ds_bpermute_b32 v38, v127, v56
	ds_bpermute_b32 v39, v129, v56
	ds_bpermute_b32 v42, v131, v56
	ds_bpermute_b32 v43, v133, v56
	ds_bpermute_b32 v26, v123, v56
	ds_bpermute_b32 v27, v125, v56
	ds_bpermute_b32 v46, v135, v56
	ds_bpermute_b32 v47, v137, v56
	s_waitcnt vmcnt(0) lgkmcnt(0)
	v_mov_b32_e32 v31, v4
	v_mov_b32_e32 v4, v3
	v_mov_b32_e32 v30, v2
	v_pk_add_f32 v[32:33], v[4:5], v[28:29]
	v_mov_b32_e32 v2, v236
	v_mov_b32_e32 v3, v237
	v_mov_b32_e32 v4, v238
	v_mov_b32_e32 v5, v239
	v_pk_add_f32 v[30:31], v[30:31], v[26:27]
	s_waitcnt vmcnt(0) lgkmcnt(0)
	v_mov_b32_e32 v37, v4
	v_mov_b32_e32 v4, v3
	v_mov_b32_e32 v36, v2
	v_pk_add_f32 v[40:41], v[4:5], v[34:35]
	v_mov_b32_e32 v2, v240
	v_mov_b32_e32 v3, v241
	v_mov_b32_e32 v4, v242
	v_mov_b32_e32 v5, v243
	v_pk_add_f32 v[48:49], v[36:37], v[38:39]
	ds_bpermute_b32 v36, v132, v56
	ds_bpermute_b32 v37, v134, v56
	v_add_f32_e32 v57, v32, v31
	v_add_f32_e32 v58, v40, v49
	s_waitcnt vmcnt(0) lgkmcnt(0)
	v_mov_b32_e32 v44, v2
	v_mov_b32_e32 v45, v4
	v_mov_b32_e32 v4, v3
	v_pk_add_f32 v[50:51], v[44:45], v[42:43]
	v_pk_add_f32 v[44:45], v[4:5], v[36:37]
	v_mov_b32_e32 v2, v244
	v_mov_b32_e32 v3, v245
	v_mov_b32_e32 v4, v235
	v_mov_b32_e32 v5, v147
	ds_bpermute_b32 v52, v136, v56
	ds_bpermute_b32 v53, v138, v56
	v_add_f32_e32 v56, v30, v31
	v_add_f32_e32 v59, v44, v51
	s_waitcnt vmcnt(0) lgkmcnt(0)
	v_mov_b32_e32 v55, v4
	v_mov_b32_e32 v4, v3
	v_mov_b32_e32 v54, v2
	v_pk_add_f32 v[2:3], v[4:5], v[52:53]
	v_pk_add_f32 v[4:5], v[30:31], v[32:33]
	v_pk_add_f32 v[54:55], v[54:55], v[46:47]
	v_max_f32_e32 v4, v4, v56
	v_add_f32_e32 v56, v30, v33
	v_max_f32_e32 v56, v56, v57
	v_add_f32_e32 v57, v32, v33
	v_max_f32_e32 v5, v57, v5
	v_max3_f32 v56, v4, v56, v5
	v_pk_add_f32 v[4:5], v[48:49], v[40:41]
	v_add_f32_e32 v57, v48, v49
	v_max_f32_e32 v4, v4, v57
	v_add_f32_e32 v57, v48, v41
	v_max_f32_e32 v57, v57, v58
	v_add_f32_e32 v58, v40, v41
	v_max_f32_e32 v5, v58, v5
	v_max3_f32 v57, v4, v57, v5
	v_pk_add_f32 v[4:5], v[50:51], v[44:45]
	v_add_f32_e32 v58, v50, v51
	v_max_f32_e32 v4, v4, v58
	v_add_f32_e32 v58, v50, v45
	v_max_f32_e32 v58, v58, v59
	v_add_f32_e32 v59, v44, v45
	v_max_f32_e32 v5, v59, v5
	v_max3_f32 v58, v4, v58, v5
	v_pk_add_f32 v[4:5], v[54:55], v[2:3]
	v_add_f32_e32 v59, v54, v55
	v_max_f32_e32 v4, v4, v59
	v_add_f32_e32 v59, v54, v3
	v_add_f32_e32 v60, v2, v55
	v_max_f32_e32 v59, v59, v60
	v_add_f32_e32 v60, v2, v3
	v_cmp_gt_f32_e32 vcc, v57, v56
	v_max_f32_e32 v5, v60, v5
	v_max3_f32 v4, v4, v59, v5
	v_cndmask_b32_e32 v56, v56, v57, vcc
	v_cndmask_b32_e64 v5, 0, 1, vcc
	v_cmp_gt_f32_e32 vcc, v58, v56
	s_nop 1
	v_cndmask_b32_e32 v56, v56, v58, vcc
	v_cndmask_b32_e64 v5, v5, 2, vcc
	v_cmp_ngt_f32_e32 vcc, v4, v56
	s_nop 1
	v_cndmask_b32_e32 v4, 3, v5, vcc
	v_cmp_ne_u32_e32 vcc, 0, v4
	s_and_saveexec_b64 s[2:3], vcc
	s_cbranch_execz .LBB0_879
	v_cmp_lt_i32_e64 s[0:1], 1, v4
	s_and_saveexec_b64 s[10:11], s[0:1]
	s_cbranch_execz .LBB0_816
	v_cmp_ne_u32_e64 s[0:1], 2, v4
	v_mov_b32_e32 v48, v50
	s_and_saveexec_b64 s[8:9], s[0:1]
	s_xor_b64 s[0:1], exec, s[8:9]
	v_mov_b32_e32 v48, v54
	s_andn2_saveexec_b64 s[0:1], s[0:1]
	s_or_b64 exec, exec, s[0:1]

; #define LAS __attribute__((address_space(3)))
; __device__ __forceinline__ void route_row(float mylg, const float* br, int row, int ai0, int lane, LAS int* asg_e, LAS int* asg_d, LAS float* asg_g) {
;     const float myaff = 1.0f / (1.0f + expf(-mylg));
;     float aff[16], sel[16];
; #pragma unroll
;     for (int e = 0; e < 16; ++e) { aff[e] = __shfl(myaff, e); sel[e] = aff[e] + br[e]; }
;     float gs[4];
; #pragma unroll
;     for (int q = 0; q < 4; ++q) { const float s0 = sel[4 * q], s1 = sel[4 * q + 1], s2 = sel[4 * q + 2], s3 = sel[4 * q + 3];
;         gs[q] = fmaxf(fmaxf(fmaxf(s0 + s1, s0 + s2), fmaxf(s0 + s3, s1 + s2)), fmaxf(s1 + s3, s2 + s3)); }
;     int best = 0; float bs = gs[0];
; #pragma unroll
;     for (int q = 1; q < 4; ++q) if (gs[q] > bs) { bs = gs[q]; best = q; }
;     float cs[4], ca[4];
; #pragma unroll
;     for (int i = 0; i < 4; ++i) { cs[i] = best == 0 ? sel[i] : best == 1 ? sel[4 + i] : best == 2 ? sel[8 + i] : sel[12 + i]; ca[i] = best == 0 ? aff[i] : best == 1 ? aff[4 + i] : best == 2 ? aff[8 + i] : aff[12 + i]; }
.LBB0_838:
	s_and_b64 vcc, exec, s[48:49]
	s_cbranch_vccnz .LBB0_866
	v_mul_f32_e32 v2, 0xbfb8aa3b, v86
	v_rndne_f32_e32 v3, v2
	s_mov_b32 s0, 0xbfb8aa3b
	v_sub_f32_e32 v4, v2, v3
	v_fma_f32 v2, v86, s0, -v2
	v_fmac_f32_e32 v2, 0xb2a5705f, v86
	v_add_f32_e32 v2, v4, v2
	v_exp_f32_e32 v2, v2
	v_cvt_i32_f32_e32 v3, v3
	s_mov_b32 s0, 0x42ce8ed0
	v_cmp_nlt_f32_e32 vcc, s0, v86
	s_mov_b32 s0, 0xc2b17218
	v_ldexp_f32 v2, v2, v3
	v_cndmask_b32_e32 v2, 0, v2, vcc
	v_cmp_ngt_f32_e32 vcc, s0, v86
	v_mov_b64_e32 v[52:53], s[28:29]
	s_nop 0
	v_cndmask_b32_e32 v2, v231, v2, vcc
	v_add_f32_e32 v2, 1.0, v2
	v_div_scale_f32 v3, s[0:1], v2, v2, 1.0
	v_rcp_f32_e32 v4, v3
	s_nop 0
	v_fma_f32 v5, -v3, v4, 1.0
	v_fmac_f32_e32 v4, v5, v4
	v_div_scale_f32 v5, vcc, 1.0, v2, 1.0
	v_mul_f32_e32 v26, v5, v4
	v_fma_f32 v27, -v3, v26, v5
	v_fmac_f32_e32 v26, v27, v4
	v_fma_f32 v3, -v3, v26, v5
	v_div_fmas_f32 v3, v3, v4, v26
	v_div_fixup_f32 v56, v3, v2, 1.0
	v_mov_b32_e32 v2, v218
	v_mov_b32_e32 v3, v219
	v_mov_b32_e32 v4, v220
	v_mov_b32_e32 v5, v221
	ds_bpermute_b32 v28, v124, v56
	ds_bpermute_b32 v29, v126, v56
	ds_bpermute_b32 v34, v128, v56
	ds_bpermute_b32 v35, v130, v56
	ds_bpermute_b32 v38, v127, v56
	ds_bpermute_b32 v39, v129, v56
	ds_bpermute_b32 v42, v131, v56
	ds_bpermute_b32 v43, v133, v56
	ds_bpermute_b32 v26, v123, v56
	ds_bpermute_b32 v27, v125, v56
	ds_bpermute_b32 v46, v135, v56
	ds_bpermute_b32 v47, v137, v56
	s_waitcnt vmcnt(0) lgkmcnt(0)
	v_mov_b32_e32 v31, v4
	v_mov_b32_e32 v4, v3
	v_mov_b32_e32 v30, v2
	v_pk_add_f32 v[32:33], v[4:5], v[28:29]
	v_mov_b32_e32 v2, v236
	v_mov_b32_e32 v3, v237
	v_mov_b32_e32 v4, v238
	v_mov_b32_e32 v5, v239
	v_pk_add_f32 v[30:31], v[30:31], v[26:27]
	s_waitcnt vmcnt(0) lgkmcnt(0)
	v_mov_b32_e32 v37, v4
	v_mov_b32_e32 v4, v3
	v_mov_b32_e32 v36, v2
	v_pk_add_f32 v[40:41], v[4:5], v[34:35]
	v_mov_b32_e32 v2, v240
	v_mov_b32_e32 v3, v241
	v_mov_b32_e32 v4, v242
	v_mov_b32_e32 v5, v243
	v_pk_add_f32 v[48:49], v[36:37], v[38:39]
	ds_bpermute_b32 v36, v132, v56
	ds_bpermute_b32 v37, v134, v56
	v_add_f32_e32 v57, v32, v31
	v_add_f32_e32 v58, v40, v49
	s_waitcnt vmcnt(0) lgkmcnt(0)
	v_mov_b32_e32 v44, v2
	v_mov_b32_e32 v45, v4
	v_mov_b32_e32 v4, v3
	v_pk_add_f32 v[50:51], v[44:45], v[42:43]
	v_pk_add_f32 v[44:45], v[4:5], v[36:37]
	v_mov_b32_e32 v2, v244
	v_mov_b32_e32 v3, v245
	v_mov_b32_e32 v4, v235
	v_mov_b32_e32 v5, v147
	ds_bpermute_b32 v52, v136, v56
	ds_bpermute_b32 v53, v138, v56
	v_add_f32_e32 v56, v30, v31
	v_add_f32_e32 v59, v44, v51
	s_waitcnt vmcnt(0) lgkmcnt(0)
	v_mov_b32_e32 v55, v4
	v_mov_b32_e32 v4, v3
	v_mov_b32_e32 v54, v2
	v_pk_add_f32 v[2:3], v[4:5], v[52:53]
	v_pk_add_f32 v[4:5], v[30:31], v[32:33]
	v_pk_add_f32 v[54:55], v[54:55], v[46:47]
	v_max_f32_e32 v4, v4, v56
	v_add_f32_e32 v56, v30, v33
	v_max_f32_e32 v56, v56, v57
	v_add_f32_e32 v57, v32, v33
	v_max_f32_e32 v5, v57, v5
	v_max3_f32 v56, v4, v56, v5
	v_pk_add_f32 v[4:5], v[48:49], v[40:41]
	v_add_f32_e32 v57, v48, v49
	v_max_f32_e32 v4, v4, v57
	v_add_f32_e32 v57, v48, v41
	v_max_f32_e32 v57, v57, v58
	v_add_f32_e32 v58, v40, v41
	v_max_f32_e32 v5, v58, v5
	v_max3_f32 v57, v4, v57, v5
	v_pk_add_f32 v[4:5], v[50:51], v[44:45]
	v_add_f32_e32 v58, v50, v51
	v_max_f32_e32 v4, v4, v58
	v_add_f32_e32 v58, v50, v45
	v_max_f32_e32 v58, v58, v59
	v_add_f32_e32 v59, v44, v45
	v_max_f32_e32 v5, v59, v5
	v_max3_f32 v58, v4, v58, v5
	v_pk_add_f32 v[4:5], v[54:55], v[2:3]
	v_add_f32_e32 v59, v54, v55
	v_max_f32_e32 v4, v4, v59
	v_add_f32_e32 v59, v54, v3
	v_add_f32_e32 v60, v2, v55
	v_max_f32_e32 v59, v59, v60
	v_add_f32_e32 v60, v2, v3
	v_cmp_gt_f32_e32 vcc, v57, v56
	v_max_f32_e32 v5, v60, v5
	v_max3_f32 v4, v4, v59, v5
	v_cndmask_b32_e32 v56, v56, v57, vcc
	v_cndmask_b32_e64 v5, 0, 1, vcc
	v_cmp_gt_f32_e32 vcc, v58, v56
	s_nop 1
	v_cndmask_b32_e32 v56, v56, v58, vcc
	v_cndmask_b32_e64 v5, v5, 2, vcc
	v_cmp_ngt_f32_e32 vcc, v4, v56
	s_nop 1
	v_cndmask_b32_e32 v4, 3, v5, vcc
	v_cmp_ne_u32_e32 vcc, 0, v4
	s_and_saveexec_b64 s[2:3], vcc
	s_cbranch_execz .LBB0_909
	v_cmp_lt_i32_e64 s[0:1], 1, v4
	s_and_saveexec_b64 s[10:11], s[0:1]
	s_cbranch_execz .LBB0_844
	v_cmp_ne_u32_e64 s[0:1], 2, v4
	v_mov_b32_e32 v48, v50
	s_and_saveexec_b64 s[8:9], s[0:1]
	s_xor_b64 s[0:1], exec, s[8:9]
	v_mov_b32_e32 v48, v54
	s_andn2_saveexec_b64 s[0:1], s[0:1]
	s_or_b64 exec, exec, s[0:1]

; __device__ __forceinline__ void unpack8h(const u32x4 w, float (&o)[8]) { o[0] = hlo(w.x); o[1] = hhi(w.x); o[2] = hlo(w.y); o[3] = hhi(w.y); o[4] = hlo(w.z); o[5] = hhi(w.z); o[6] = hlo(w.w); o[7] = hhi(w.w); }
; __device__ __forceinline__ void unpack8(const u32x4 w, float (&o)[8]) { o[0] = bflo(w.x); o[1] = bfhi(w.x); o[2] = bflo(w.y); o[3] = bfhi(w.y); o[4] = bflo(w.z); o[5] = bfhi(w.z); o[6] = bflo(w.w); o[7] = bfhi(w.w); }
; __device__ __forceinline__ void ln_rows(float (&v)[4][8], const float* g, const float* bta, int lane) {
;     float s = 0.f;
; #pragma unroll
;     for (int j = 0; j < 4; ++j)
; #pragma unroll
;         for (int e = 0; e < 8; ++e) s += v[j][e];
;     const float mean = wave_sum(s) * (1.f / DM); float q = 0.f;
; __device__ __forceinline__ void ln2_phase(const Args& a, Frame& F, int l) {
;     ...
;         for (int j = 0; j < 4; ++j) { float y0[8], y1[8];
;             unpack8h(rp[j], v[j]); unpack8(ry0[j], y0); unpack8(ry1[j], y1);
; #pragma unroll
;             for (int e = 0; e < 8; ++e) v[j][e] += y0[e] + y1[e]; }
.LBB0_1295:
	v_cvt_f32_f16_sdwa v119, v86 dst_sel:DWORD dst_unused:UNUSED_PAD src0_sel:WORD_1
	v_cvt_f32_f16_e32 v118, v86
	v_lshlrev_b32_e32 v126, 16, v90
	v_and_b32_e32 v127, 0xffff0000, v90
	v_lshlrev_b32_e32 v128, 16, v94
	v_and_b32_e32 v129, 0xffff0000, v94
	v_pk_add_f32 v[126:127], v[126:127], v[128:129]
	v_lshlrev_b32_e32 v86, 16, v91
	v_pk_add_f32 v[118:119], v[126:127], v[118:119]
	v_cvt_f32_f16_sdwa v127, v87 dst_sel:DWORD dst_unused:UNUSED_PAD src0_sel:WORD_1
	v_cvt_f32_f16_e32 v126, v87
	v_and_b32_e32 v87, 0xffff0000, v91
	v_lshlrev_b32_e32 v90, 16, v95
	v_and_b32_e32 v91, 0xffff0000, v95
	v_pk_add_f32 v[86:87], v[86:87], v[90:91]
	v_cvt_f32_f16_sdwa v91, v88 dst_sel:DWORD dst_unused:UNUSED_PAD src0_sel:WORD_1
	v_cvt_f32_f16_e32 v90, v88
	v_pk_add_f32 v[86:87], v[86:87], v[126:127]
	v_lshlrev_b32_e32 v94, 16, v92
	v_and_b32_e32 v95, 0xffff0000, v92
	v_lshlrev_b32_e32 v126, 16, v96
	v_and_b32_e32 v127, 0xffff0000, v96
	v_pk_add_f32 v[94:95], v[94:95], v[126:127]
	v_lshlrev_b32_e32 v88, 16, v93
	v_pk_add_f32 v[90:91], v[94:95], v[90:91]
	v_cvt_f32_f16_sdwa v95, v89 dst_sel:DWORD dst_unused:UNUSED_PAD src0_sel:WORD_1
	v_cvt_f32_f16_e32 v94, v89
	v_and_b32_e32 v89, 0xffff0000, v93
	v_lshlrev_b32_e32 v92, 16, v97
	v_and_b32_e32 v93, 0xffff0000, v97
	v_pk_add_f32 v[88:89], v[88:89], v[92:93]
	v_cvt_f32_f16_sdwa v93, v82 dst_sel:DWORD dst_unused:UNUSED_PAD src0_sel:WORD_1
	v_cvt_f32_f16_e32 v92, v82
	v_pk_add_f32 v[88:89], v[88:89], v[94:95]
	v_lshlrev_b32_e32 v94, 16, v74
	v_and_b32_e32 v95, 0xffff0000, v74
	v_lshlrev_b32_e32 v96, 16, v78
	v_and_b32_e32 v97, 0xffff0000, v78
	v_pk_add_f32 v[94:95], v[94:95], v[96:97]
	v_lshlrev_b32_e32 v74, 16, v75
	v_pk_add_f32 v[92:93], v[94:95], v[92:93]
	v_cvt_f32_f16_sdwa v95, v83 dst_sel:DWORD dst_unused:UNUSED_PAD src0_sel:WORD_1
	v_cvt_f32_f16_e32 v94, v83
	v_and_b32_e32 v75, 0xffff0000, v75
	v_lshlrev_b32_e32 v78, 16, v79
	v_and_b32_e32 v79, 0xffff0000, v79
	v_pk_add_f32 v[74:75], v[74:75], v[78:79]
	v_cvt_f32_f16_sdwa v79, v84 dst_sel:DWORD dst_unused:UNUSED_PAD src0_sel:WORD_1
	v_cvt_f32_f16_e32 v78, v84
	v_pk_add_f32 v[74:75], v[74:75], v[94:95]
	v_lshlrev_b32_e32 v82, 16, v76
	v_and_b32_e32 v83, 0xffff0000, v76
	v_lshlrev_b32_e32 v94, 16, v80
	v_and_b32_e32 v95, 0xffff0000, v80
	v_pk_add_f32 v[82:83], v[82:83], v[94:95]
	v_lshlrev_b32_e32 v76, 16, v77
	v_pk_add_f32 v[78:79], v[82:83], v[78:79]
	v_cvt_f32_f16_sdwa v83, v85 dst_sel:DWORD dst_unused:UNUSED_PAD src0_sel:WORD_1
	v_cvt_f32_f16_e32 v82, v85
	v_and_b32_e32 v77, 0xffff0000, v77
	v_lshlrev_b32_e32 v80, 16, v81
	v_and_b32_e32 v81, 0xffff0000, v81
	v_pk_add_f32 v[76:77], v[76:77], v[80:81]
	v_cvt_f32_f16_sdwa v81, v70 dst_sel:DWORD dst_unused:UNUSED_PAD src0_sel:WORD_1
	v_cvt_f32_f16_e32 v80, v70
	v_pk_add_f32 v[76:77], v[76:77], v[82:83]
	v_lshlrev_b32_e32 v82, 16, v62
	v_and_b32_e32 v83, 0xffff0000, v62
	v_lshlrev_b32_e32 v84, 16, v66
	v_and_b32_e32 v85, 0xffff0000, v66
	v_pk_add_f32 v[82:83], v[82:83], v[84:85]
	v_add_f32_e32 v0, 0, v118
	v_pk_add_f32 v[80:81], v[82:83], v[80:81]
	v_cvt_f32_f16_sdwa v83, v71 dst_sel:DWORD dst_unused:UNUSED_PAD src0_sel:WORD_1
	v_cvt_f32_f16_e32 v82, v71
	v_add_f32_e32 v0, v119, v0
	v_add_f32_e32 v0, v86, v0
	v_lshlrev_b32_e32 v62, 16, v63
	v_and_b32_e32 v63, 0xffff0000, v63
	v_lshlrev_b32_e32 v66, 16, v67
	v_and_b32_e32 v67, 0xffff0000, v67
	v_add_f32_e32 v0, v87, v0
	v_pk_add_f32 v[62:63], v[62:63], v[66:67]
	v_add_f32_e32 v0, v90, v0
	v_pk_add_f32 v[66:67], v[62:63], v[82:83]
	v_cvt_f32_f16_sdwa v63, v72 dst_sel:DWORD dst_unused:UNUSED_PAD src0_sel:WORD_1
	v_cvt_f32_f16_e32 v62, v72
	v_add_f32_e32 v0, v91, v0
	v_add_f32_e32 v0, v88, v0
	v_lshlrev_b32_e32 v70, 16, v64
	v_and_b32_e32 v71, 0xffff0000, v64
	v_lshlrev_b32_e32 v82, 16, v68
	v_and_b32_e32 v83, 0xffff0000, v68
	v_add_f32_e32 v0, v89, v0
	v_pk_add_f32 v[70:71], v[70:71], v[82:83]
	v_add_f32_e32 v0, v92, v0
	v_pk_add_f32 v[70:71], v[70:71], v[62:63]
	v_cvt_f32_f16_sdwa v63, v73 dst_sel:DWORD dst_unused:UNUSED_PAD src0_sel:WORD_1
	v_cvt_f32_f16_e32 v62, v73
	v_add_f32_e32 v0, v93, v0
	v_add_f32_e32 v0, v74, v0
	v_lshlrev_b32_e32 v64, 16, v65
	v_and_b32_e32 v65, 0xffff0000, v65
	v_lshlrev_b32_e32 v68, 16, v69
	v_and_b32_e32 v69, 0xffff0000, v69
	v_add_f32_e32 v0, v75, v0
	v_pk_add_f32 v[64:65], v[64:65], v[68:69]
	v_add_f32_e32 v0, v78, v0
	v_pk_add_f32 v[68:69], v[64:65], v[62:63]
	v_cvt_f32_f16_sdwa v63, v58 dst_sel:DWORD dst_unused:UNUSED_PAD src0_sel:WORD_1
	v_cvt_f32_f16_e32 v62, v58
	v_add_f32_e32 v0, v79, v0
	v_add_f32_e32 v0, v76, v0
	v_lshlrev_b32_e32 v64, 16, v50
	v_and_b32_e32 v65, 0xffff0000, v50
	v_lshlrev_b32_e32 v72, 16, v54
	v_and_b32_e32 v73, 0xffff0000, v54
	v_add_f32_e32 v0, v77, v0
	v_pk_add_f32 v[64:65], v[64:65], v[72:73]
	v_add_f32_e32 v0, v80, v0
	v_pk_add_f32 v[72:73], v[64:65], v[62:63]
	v_cvt_f32_f16_sdwa v63, v59 dst_sel:DWORD dst_unused:UNUSED_PAD src0_sel:WORD_1
	v_cvt_f32_f16_e32 v62, v59
	v_add_f32_e32 v0, v81, v0
	v_add_f32_e32 v0, v66, v0
	v_lshlrev_b32_e32 v50, 16, v51
	v_and_b32_e32 v51, 0xffff0000, v51
	v_lshlrev_b32_e32 v54, 16, v55
	v_and_b32_e32 v55, 0xffff0000, v55
	v_add_f32_e32 v0, v67, v0
	v_pk_add_f32 v[50:51], v[50:51], v[54:55]
	v_add_f32_e32 v0, v70, v0
	v_pk_add_f32 v[82:83], v[50:51], v[62:63]
	v_cvt_f32_f16_sdwa v51, v60 dst_sel:DWORD dst_unused:UNUSED_PAD src0_sel:WORD_1
	v_cvt_f32_f16_e32 v50, v60
	v_add_f32_e32 v0, v71, v0
	v_add_f32_e32 v0, v68, v0
	v_lshlrev_b32_e32 v54, 16, v52
	v_and_b32_e32 v55, 0xffff0000, v52
	v_lshlrev_b32_e32 v58, 16, v56
	v_and_b32_e32 v59, 0xffff0000, v56
	v_add_f32_e32 v0, v69, v0
	v_pk_add_f32 v[54:55], v[54:55], v[58:59]
	v_add_f32_e32 v0, v72, v0
	v_pk_add_f32 v[84:85], v[54:55], v[50:51]
	v_cvt_f32_f16_sdwa v51, v61 dst_sel:DWORD dst_unused:UNUSED_PAD src0_sel:WORD_1
	v_cvt_f32_f16_e32 v50, v61
	v_add_f32_e32 v0, v73, v0
	v_add_f32_e32 v0, v82, v0
	v_lshlrev_b32_e32 v52, 16, v53
	v_and_b32_e32 v53, 0xffff0000, v53
	v_lshlrev_b32_e32 v54, 16, v57
	v_and_b32_e32 v55, 0xffff0000, v57
	v_add_f32_e32 v0, v83, v0
	v_pk_add_f32 v[52:53], v[52:53], v[54:55]
	v_add_f32_e32 v0, v84, v0
	v_pk_add_f32 v[94:95], v[52:53], v[50:51]
	v_add_f32_e32 v0, v85, v0
	v_add_f32_e32 v0, v94, v0
	v_add_f32_e32 v0, v95, v0
	s_mov_b32 s0, 0xf800000
	s_waitcnt lgkmcnt(0)
; #define GAS __attribute__((address_space(1)))
; __device__ __forceinline__ void ln_rows(float (&v)[4][8], const float* g, const float* bta, int lane) {
;     ...
;     const float mean = wave_sum(s) * (1.f / DM); float q = 0.f;
; #pragma unroll
;     for (int j = 0; j < 4; ++j)
; #pragma unroll
;         for (int e = 0; e < 8; ++e) { v[j][e] -= mean; q += v[j][e] * v[j][e]; }
;     const float rstd = 1.0f / sqrtf(wave_sum(q) * (1.f / DM) + LN_EPS);
; #pragma unroll
;     for (int j = 0; j < 4; ++j) { const f32x4 g0 = *(const GAS f32x4*)(g + 8 * lane + 512 * j), g1 = *(const GAS f32x4*)(g + 8 * lane + 512 * j + 4), b0 = *(const GAS f32x4*)(bta + 8 * lane + 512 * j), b1 = *(const GAS f32x4*)(bta + 8 * lane + 512 * j + 4);
	v_add_f32_dpp v0, v0, v0 quad_perm:[1,0,3,2] row_mask:0xf bank_mask:0xf
	s_waitcnt lgkmcnt(0)
	s_nop 0
	v_add_f32_dpp v0, v0, v0 quad_perm:[2,3,0,1] row_mask:0xf bank_mask:0xf
	s_waitcnt lgkmcnt(0)
	s_nop 0
	v_add_f32_dpp v0, v0, v0 row_half_mirror row_mask:0xf bank_mask:0xf
	s_waitcnt lgkmcnt(0)
	s_nop 0
	v_add_f32_dpp v0, v0, v0 row_mirror row_mask:0xf bank_mask:0xf
	s_waitcnt lgkmcnt(0)
	v_mov_b32_e32 v50, v0
	s_nop 1
	v_permlane16_swap_b32_e32 v0, v50
	v_add_f32_e32 v0, v0, v50
	s_waitcnt lgkmcnt(0)
	v_mov_b32_e32 v50, v0
	s_nop 1
	v_permlane32_swap_b32_e32 v0, v50
	v_add_f32_e32 v0, v0, v50
	v_mul_f32_e32 v0, 0x3a000000, v0
	v_pk_add_f32 v[118:119], v[118:119], v[0:1] op_sel_hi:[1,0] neg_lo:[0,1] neg_hi:[0,1]
	v_pk_add_f32 v[152:153], v[86:87], v[0:1] op_sel_hi:[1,0] neg_lo:[0,1] neg_hi:[0,1]
	v_pk_mul_f32 v[96:97], v[118:119], v[118:119]
	v_pk_add_f32 v[150:151], v[90:91], v[0:1] op_sel_hi:[1,0] neg_lo:[0,1] neg_hi:[0,1]
	v_pk_mul_f32 v[86:87], v[152:153], v[152:153]
	v_pk_add_f32 v[154:155], v[88:89], v[0:1] op_sel_hi:[1,0] neg_lo:[0,1] neg_hi:[0,1]
	v_pk_add_f32 v[156:157], v[92:93], v[0:1] op_sel_hi:[1,0] neg_lo:[0,1] neg_hi:[0,1]
	v_pk_add_f32 v[158:159], v[78:79], v[0:1] op_sel_hi:[1,0] neg_lo:[0,1] neg_hi:[0,1]
	v_pk_add_f32 v[160:161], v[74:75], v[0:1] op_sel_hi:[1,0] neg_lo:[0,1] neg_hi:[0,1]
	v_pk_add_f32 v[162:163], v[76:77], v[0:1] op_sel_hi:[1,0] neg_lo:[0,1] neg_hi:[0,1]
	v_pk_add_f32 v[164:165], v[80:81], v[0:1] op_sel_hi:[1,0] neg_lo:[0,1] neg_hi:[0,1]
	v_pk_add_f32 v[166:167], v[70:71], v[0:1] op_sel_hi:[1,0] neg_lo:[0,1] neg_hi:[0,1]
	v_pk_add_f32 v[168:169], v[66:67], v[0:1] op_sel_hi:[1,0] neg_lo:[0,1] neg_hi:[0,1]
	v_pk_add_f32 v[170:171], v[68:69], v[0:1] op_sel_hi:[1,0] neg_lo:[0,1] neg_hi:[0,1]
	v_pk_add_f32 v[172:173], v[72:73], v[0:1] op_sel_hi:[1,0] neg_lo:[0,1] neg_hi:[0,1]
	v_pk_add_f32 v[174:175], v[84:85], v[0:1] op_sel_hi:[1,0] neg_lo:[0,1] neg_hi:[0,1]
	v_pk_add_f32 v[176:177], v[82:83], v[0:1] op_sel_hi:[1,0] neg_lo:[0,1] neg_hi:[0,1]
	v_pk_add_f32 v[178:179], v[94:95], v[0:1] op_sel_hi:[1,0] neg_lo:[0,1] neg_hi:[0,1]
	v_add_f32_e32 v0, v96, v97
	v_add_f32_e32 v0, v86, v0
	v_pk_mul_f32 v[90:91], v[150:151], v[150:151]
	v_add_f32_e32 v0, v87, v0
	v_add_f32_e32 v0, v90, v0
	v_pk_mul_f32 v[88:89], v[154:155], v[154:155]
	v_add_f32_e32 v0, v91, v0
	v_add_f32_e32 v0, v88, v0
	v_pk_mul_f32 v[92:93], v[156:157], v[156:157]
	v_add_f32_e32 v0, v89, v0
	v_add_f32_e32 v0, v92, v0
	v_pk_mul_f32 v[74:75], v[160:161], v[160:161]
	v_add_f32_e32 v0, v93, v0
	v_add_f32_e32 v0, v74, v0
	v_pk_mul_f32 v[78:79], v[158:159], v[158:159]
	v_add_f32_e32 v0, v75, v0
	v_add_f32_e32 v0, v78, v0
	v_pk_mul_f32 v[76:77], v[162:163], v[162:163]
	v_add_f32_e32 v0, v79, v0
	v_add_f32_e32 v0, v76, v0
	v_pk_mul_f32 v[80:81], v[164:165], v[164:165]
	v_add_f32_e32 v0, v77, v0
	v_add_f32_e32 v0, v80, v0
	v_pk_mul_f32 v[66:67], v[168:169], v[168:169]
	v_add_f32_e32 v0, v81, v0
	v_add_f32_e32 v0, v66, v0
	v_pk_mul_f32 v[70:71], v[166:167], v[166:167]
	v_add_f32_e32 v0, v67, v0
	v_add_f32_e32 v0, v70, v0
	v_pk_mul_f32 v[68:69], v[170:171], v[170:171]
	v_add_f32_e32 v0, v71, v0
	v_add_f32_e32 v0, v68, v0
	v_pk_mul_f32 v[72:73], v[172:173], v[172:173]
	v_add_f32_e32 v0, v69, v0
	v_add_f32_e32 v0, v72, v0
	v_pk_mul_f32 v[82:83], v[176:177], v[176:177]
	v_add_f32_e32 v0, v73, v0
	v_add_f32_e32 v0, v82, v0
	global_load_dwordx4 v[50:53], v[102:103], off offset:16
	global_load_dwordx4 v[54:57], v[102:103], off
	global_load_dwordx4 v[58:61], v[104:105], off offset:16
	global_load_dwordx4 v[62:65], v[104:105], off
	v_pk_mul_f32 v[84:85], v[174:175], v[174:175]
	v_add_f32_e32 v0, v83, v0
	v_add_f32_e32 v0, v84, v0
	v_pk_mul_f32 v[94:95], v[178:179], v[178:179]
	v_add_f32_e32 v0, v85, v0
	global_load_dwordx4 v[66:69], v[102:103], off offset:2064
	global_load_dwordx4 v[70:73], v[102:103], off offset:2048
	global_load_dwordx4 v[82:85], v[104:105], off offset:2048
	global_load_dwordx4 v[86:89], v[104:105], off offset:2064
	v_add_f32_e32 v0, v94, v0
	v_add_f32_e32 v0, v95, v0
	global_load_dwordx4 v[90:93], v[106:107], off offset:16
	global_load_dwordx4 v[94:97], v[106:107], off
	global_load_dwordx4 v[126:129], v[108:109], off offset:16
	global_load_dwordx4 v[130:133], v[108:109], off
	global_load_dwordx4 v[134:137], v[110:111], off offset:16
	global_load_dwordx4 v[138:141], v[110:111], off
	global_load_dwordx4 v[142:145], v[112:113], off
	global_load_dwordx4 v[146:149], v[112:113], off offset:16
	s_waitcnt lgkmcnt(0)
; #define GAS __attribute__((address_space(1)))
; __device__ __forceinline__ void ln_rows(float (&v)[4][8], const float* g, const float* bta, int lane) {
;     ...
;     const float rstd = 1.0f / sqrtf(wave_sum(q) * (1.f / DM) + LN_EPS);
; #pragma unroll
;     for (int j = 0; j < 4; ++j) { const f32x4 g0 = *(const GAS f32x4*)(g + 8 * lane + 512 * j), g1 = *(const GAS f32x4*)(g + 8 * lane + 512 * j + 4), b0 = *(const GAS f32x4*)(bta + 8 * lane + 512 * j), b1 = *(const GAS f32x4*)(bta + 8 * lane + 512 * j + 4);
; #pragma unroll
;         for (int e = 0; e < 4; ++e) { v[j][e] = v[j][e] * rstd * g0[e] + b0[e]; v[j][4 + e] = v[j][4 + e] * rstd * g1[e] + b1[e]; } }
; __device__ __forceinline__ void ln2_phase(const Args& a, Frame& F, int l) {
;     ...
;         if (l == DEPTH - 1) {
; #pragma unroll
;             for (int j = 0; j < 4; ++j) { *(GAS f32x4*)(out + (size_t)row * DM + 8 * lane + 512 * j) = (f32x4){v[j][0], v[j][1], v[j][2], v[j][3]}; *(GAS f32x4*)(out + (size_t)row * DM + 8 * lane + 512 * j + 4) = (f32x4){v[j][4], v[j][5], v[j][6], v[j][7]}; }
	v_add_f32_dpp v0, v0, v0 quad_perm:[1,0,3,2] row_mask:0xf bank_mask:0xf
	s_waitcnt lgkmcnt(0)
	s_nop 0
	v_add_f32_dpp v0, v0, v0 quad_perm:[2,3,0,1] row_mask:0xf bank_mask:0xf
	s_waitcnt lgkmcnt(0)
	s_nop 0
	v_add_f32_dpp v0, v0, v0 row_half_mirror row_mask:0xf bank_mask:0xf
	s_waitcnt lgkmcnt(0)
	s_nop 0
	v_add_f32_dpp v0, v0, v0 row_mirror row_mask:0xf bank_mask:0xf
	s_waitcnt lgkmcnt(0)
	v_mov_b32_e32 v74, v0
	s_nop 1
	v_permlane16_swap_b32_e32 v0, v74
	v_add_f32_e32 v0, v0, v74
	s_waitcnt lgkmcnt(0)
	v_mov_b32_e32 v74, v0
	s_nop 1
	v_permlane32_swap_b32_e32 v0, v74
	v_add_f32_e32 v0, v0, v74
	v_fmamk_f32 v0, v0, 0x3a000000, v230
	v_mul_f32_e32 v74, 0x4f800000, v0
	v_cmp_gt_f32_e32 vcc, s0, v0
	s_nop 1
	v_cndmask_b32_e32 v0, v0, v74, vcc
	v_sqrt_f32_e32 v74, v0
	s_nop 0
	v_add_u32_e32 v75, -1, v74
	v_fma_f32 v76, -v75, v74, v0
	v_cmp_ge_f32_e64 s[0:1], 0, v76
	v_add_u32_e32 v76, 1, v74
	s_nop 0
	v_cndmask_b32_e64 v75, v74, v75, s[0:1]
	v_fma_f32 v74, -v76, v74, v0
	v_cmp_lt_f32_e64 s[0:1], 0, v74
	s_nop 1
	v_cndmask_b32_e64 v74, v75, v76, s[0:1]
	v_mul_f32_e32 v75, 0x37800000, v74
	v_cndmask_b32_e32 v74, v74, v75, vcc
	v_cmp_class_f32_e32 vcc, v0, v227
	s_nop 1
	v_cndmask_b32_e32 v0, v74, v0, vcc
	v_div_scale_f32 v74, s[0:1], v0, v0, 1.0
	v_rcp_f32_e32 v75, v74
	v_readlane_b32 s0, v246, 11
	v_readlane_b32 s1, v246, 12
	v_fma_f32 v76, -v74, v75, 1.0
	v_fmac_f32_e32 v75, v76, v75
	v_div_scale_f32 v76, vcc, 1.0, v0, 1.0
	v_mul_f32_e32 v77, v76, v75
	v_fma_f32 v78, -v74, v77, v76
	v_fmac_f32_e32 v77, v78, v75
	v_fma_f32 v74, -v74, v77, v76
	v_div_fmas_f32 v74, v74, v75, v77
	v_div_fixup_f32 v0, v74, v0, 1.0
	v_pk_mul_f32 v[74:75], v[118:119], v[0:1] op_sel_hi:[1,0]
	v_pk_mul_f32 v[76:77], v[150:151], v[0:1] op_sel_hi:[1,0]
	s_waitcnt vmcnt(12)
	v_pk_fma_f32 v[78:79], v[54:55], v[74:75], v[62:63]
	v_pk_fma_f32 v[74:75], v[50:51], v[76:77], v[58:59]
	v_pk_mul_f32 v[50:51], v[152:153], v[0:1] op_sel_hi:[1,0]
	v_pk_mul_f32 v[54:55], v[154:155], v[0:1] op_sel_hi:[1,0]
	v_pk_fma_f32 v[80:81], v[56:57], v[50:51], v[64:65]
	v_pk_fma_f32 v[76:77], v[52:53], v[54:55], v[60:61]
	v_pk_mul_f32 v[50:51], v[156:157], v[0:1] op_sel_hi:[1,0]
	v_pk_mul_f32 v[52:53], v[158:159], v[0:1] op_sel_hi:[1,0]
	s_waitcnt vmcnt(9)
	v_pk_fma_f32 v[70:71], v[70:71], v[50:51], v[82:83]
	s_waitcnt vmcnt(8)
	v_pk_fma_f32 v[66:67], v[66:67], v[52:53], v[86:87]
	v_pk_mul_f32 v[50:51], v[160:161], v[0:1] op_sel_hi:[1,0]
	v_pk_mul_f32 v[52:53], v[162:163], v[0:1] op_sel_hi:[1,0]
	v_pk_fma_f32 v[72:73], v[72:73], v[50:51], v[84:85]
	v_pk_fma_f32 v[68:69], v[68:69], v[52:53], v[88:89]
	v_pk_mul_f32 v[50:51], v[164:165], v[0:1] op_sel_hi:[1,0]
	v_pk_mul_f32 v[52:53], v[166:167], v[0:1] op_sel_hi:[1,0]
	s_waitcnt vmcnt(4)
	v_pk_fma_f32 v[62:63], v[94:95], v[50:51], v[130:131]
	v_pk_fma_f32 v[58:59], v[90:91], v[52:53], v[126:127]
	v_pk_mul_f32 v[50:51], v[168:169], v[0:1] op_sel_hi:[1,0]
	v_pk_mul_f32 v[52:53], v[170:171], v[0:1] op_sel_hi:[1,0]
	v_pk_fma_f32 v[64:65], v[96:97], v[50:51], v[132:133]
	v_pk_fma_f32 v[60:61], v[92:93], v[52:53], v[128:129]
	v_pk_mul_f32 v[50:51], v[172:173], v[0:1] op_sel_hi:[1,0]
	v_pk_mul_f32 v[52:53], v[174:175], v[0:1] op_sel_hi:[1,0]
	s_waitcnt vmcnt(1)
	v_pk_fma_f32 v[54:55], v[138:139], v[50:51], v[142:143]
	s_waitcnt vmcnt(0)
	v_pk_fma_f32 v[50:51], v[134:135], v[52:53], v[146:147]
	v_pk_mul_f32 v[52:53], v[176:177], v[0:1] op_sel_hi:[1,0]
	v_pk_mul_f32 v[82:83], v[178:179], v[0:1] op_sel_hi:[1,0]
	v_pk_fma_f32 v[56:57], v[140:141], v[52:53], v[144:145]
	v_pk_fma_f32 v[52:53], v[136:137], v[82:83], v[148:149]
	s_andn2_b64 vcc, exec, s[0:1]
	s_mov_b64 s[0:1], -1
	s_cbranch_vccnz .LBB0_1297
	v_add_co_u32_e32 v82, vcc, 0xfffff000, v116
	s_mov_b64 s[0:1], 0
	s_nop 0
	v_addc_co_u32_e32 v83, vcc, -1, v117, vcc
	global_store_dwordx4 v[82:83], v[78:81], off offset:-2064
	global_store_dwordx4 v[82:83], v[74:77], off offset:-2048
	global_store_dwordx4 v[82:83], v[70:73], off offset:-16
	global_store_dwordx4 v[116:117], v[66:69], off offset:-4096
	global_store_dwordx4 v[116:117], v[62:65], off offset:-2064
	global_store_dwordx4 v[116:117], v[58:61], off offset:-2048
	global_store_dwordx4 v[116:117], v[54:57], off offset:-16
	global_store_dwordx4 v[116:117], v[50:53], off
